# baseline (speedup 1.0000x reference)
_Z11gemm_kernelILi256ELi192ELi4ELi2ELi0EEvPKDF16_S1_PKfS3_PDF16_S4_S4_Pfi:
	s_lshl_b32 s3, s2, 1
	s_and_b32 s3, s3, 12
	s_bfe_u32 s12, s2, 0x20003
	s_load_dwordx8 s[4:11], s[0:1], 0x0
	s_or_b32 s17, s3, s12
	s_lshl_b32 s3, s2, 3
	s_and_b32 s3, s3, 8
	s_lshr_b32 s2, s2, 5
	s_add_i32 s2, s3, s2
	s_mulk_i32 s2, 0xc0
	s_mov_b32 s3, 0
	s_lshl_b64 s[12:13], s[2:3], 11
	s_lshl_b32 s14, s17, 19
	v_readfirstlane_b32 s16, v0
	s_nop 1
	s_lshr_b32 s22, s16, 6
	s_cmp_ge_u32 s22, 4
	s_cbranch_scc0 .Lg0_prio_done
	s_setprio 1
.Lg0_prio_done:
	s_waitcnt lgkmcnt(0)
	s_add_u32 s4, s4, s14
	v_lshlrev_b32_e32 v2, 4, v0
	s_addc_u32 s5, s5, 0
	s_bfe_i32 s18, s16, 0x10006
	v_and_b32_e32 v164, 0x70, v2
	v_lshlrev_b32_e32 v2, 8, v0
	s_and_b32 s19, s18, 0x60
	s_and_b32 s15, s18, 32
	v_lshlrev_b32_e32 v1, 7, v0
	v_mov_b32_e32 v165, 0
	v_and_b32_e32 v46, 0x1f800, v2
	s_mov_b32 s14, 0x1fc00
	v_mov_b32_e32 v2, 0x10000
	v_lshl_add_u64 v[10:11], s[4:5], 0, v[164:165]
	v_mov_b32_e32 v47, v165
	v_bitop3_b32 v2, v1, s14, v2 bitop3:0xc8
	s_mov_b32 s14, 0x3fc00
	v_mov_b32_e32 v12, 0x30000
	s_add_u32 s6, s6, s12
	v_lshl_add_u64 v[96:97], v[10:11], 0, v[46:47]
	v_lshlrev_b32_e32 v48, 1, v2
	v_mov_b32_e32 v49, v165
	v_or_b32_e32 v50, 0x40000, v46
	v_mov_b32_e32 v51, v165
	v_bitop3_b32 v1, v1, s14, v12 bitop3:0xc8
	s_addc_u32 s7, s7, s13
	v_lshl_add_u64 v[98:99], v[10:11], 0, v[48:49]
	global_load_dwordx4 v[2:5], v[96:97], off
	global_load_dwordx4 v[6:9], v[98:99], off
	v_lshl_add_u64 v[100:101], v[10:11], 0, v[50:51]
	v_lshlrev_b32_e32 v30, 1, v1
	v_mov_b32_e32 v31, v165
	v_lshl_add_u64 v[26:27], s[6:7], 0, v[164:165]
	v_lshl_add_u64 v[102:103], v[10:11], 0, v[30:31]
	global_load_dwordx4 v[10:13], v[100:101], off
	global_load_dwordx4 v[14:17], v[102:103], off
	v_lshl_add_u64 v[106:107], v[26:27], 0, v[46:47]
	v_lshl_add_u64 v[108:109], v[26:27], 0, v[48:49]
	global_load_dwordx4 v[18:21], v[106:107], off
	global_load_dwordx4 v[22:25], v[108:109], off
	v_lshl_add_u64 v[110:111], v[26:27], 0, v[50:51]
	global_load_dwordx4 v[26:29], v[110:111], off
	v_or_b32_e32 v32, 0x200, v0
	v_lshrrev_b32_e32 v65, 3, v32
	v_lshl_add_u64 v[32:33], s[4:5], 0, v[46:47]
	v_lshl_add_u64 v[30:31], s[4:5], 0, v[30:31]
	s_movk_i32 s20, 0x90
	v_lshrrev_b32_e32 v1, 3, v0
	v_add_u32_e32 v66, 0, v164
	v_lshl_add_u64 v[34:35], s[4:5], 0, v[48:49]
	v_lshl_add_u64 v[36:37], s[4:5], 0, v[50:51]
	v_lshl_add_u64 v[52:53], v[32:33], 0, v[164:165]
	v_lshl_add_u64 v[58:59], v[30:31], 0, v[164:165]
	v_lshl_add_u64 v[46:47], s[6:7], 0, v[46:47]
	v_or_b32_e32 v64, 0x600, v0
	v_mad_u32_u24 v114, v1, s20, v66
	v_lshl_add_u64 v[54:55], v[34:35], 0, v[164:165]
	v_lshl_add_u64 v[56:57], v[36:37], 0, v[164:165]
	global_load_dwordx4 v[30:33], v[52:53], off offset:128
	global_load_dwordx4 v[34:37], v[54:55], off offset:128
	global_load_dwordx4 v[38:41], v[56:57], off offset:128
	global_load_dwordx4 v[42:45], v[58:59], off offset:128
	v_lshl_add_u64 v[48:49], s[6:7], 0, v[48:49]
	v_lshl_add_u64 v[50:51], s[6:7], 0, v[50:51]
	v_lshl_add_u64 v[58:59], v[46:47], 0, v[164:165]
	v_mad_u32_u24 v115, v65, s20, v66
	v_lshl_add_u64 v[60:61], v[48:49], 0, v[164:165]
	v_lshl_add_u64 v[62:63], v[50:51], 0, v[164:165]
	global_load_dwordx4 v[46:49], v[58:59], off offset:128
	global_load_dwordx4 v[50:53], v[60:61], off offset:128
	global_load_dwordx4 v[54:57], v[62:63], off offset:128
	s_add_i32 s14, s19, s2
	s_lshr_b32 s2, s16, 1
	v_and_b32_e32 v166, 31, v0
	s_and_b32 s2, s2, 0x7fffffc0
	v_or_b32_e32 v168, s15, v166
	v_add_u32_e32 v118, 0x4800, v114
	v_or_b32_e32 v162, s19, v166
	v_lshrrev_b32_e32 v113, 1, v168
	s_waitcnt vmcnt(13)
	ds_write_b128 v114, v[2:5]
	s_waitcnt vmcnt(12)
	ds_write_b128 v115, v[6:9]
	s_waitcnt vmcnt(11)
	ds_write_b128 v114, v[10:13] offset:18432
	v_lshrrev_b32_e32 v2, 3, v64
	v_mad_u32_u24 v117, v2, s20, v66
	s_waitcnt vmcnt(10)
	ds_write_b128 v117, v[14:17]
	s_waitcnt vmcnt(9)
	ds_write_b128 v114, v[18:21] offset:36864
	s_waitcnt vmcnt(8)
	ds_write_b128 v115, v[22:25] offset:36864
	s_waitcnt vmcnt(7)
	ds_write_b128 v114, v[26:29] offset:55296
	s_waitcnt lgkmcnt(0)
	s_barrier
	global_load_dwordx4 v[122:125], v[96:97], off offset:256
	global_load_dwordx4 v[126:129], v[98:99], off offset:256
	global_load_dwordx4 v[130:133], v[100:101], off offset:256
	global_load_dwordx4 v[134:137], v[102:103], off offset:256
	global_load_dwordx4 v[138:141], v[106:107], off offset:256
	global_load_dwordx4 v[142:145], v[108:109], off offset:256
	global_load_dwordx4 v[146:149], v[110:111], off offset:256
	s_load_dwordx4 s[4:7], s[0:1], 0x20
	s_load_dwordx2 s[12:13], s[0:1], 0x30
	v_bfe_u32 v2, v0, 5, 1
	s_lshl_b32 s0, s17, 8
	s_add_i32 s1, 0, 0x18c00
	v_bitop3_b32 v3, s18, 32, v166 bitop3:0x26
	v_add_u32_e32 v5, s1, v164
	v_lshlrev_b32_e32 v121, 4, v2
	s_add_i32 s0, s2, s0
	v_lshlrev_b32_e32 v2, 2, v2
	v_and_b32_e32 v164, 1, v0
	v_or_b32_e32 v6, s2, v166
	v_add_u32_e32 v4, 0, v121
	v_or3_b32 v167, s0, v2, v164
	v_lshrrev_b32_e32 v112, 1, v3
	v_mad_u32_u24 v119, v1, s20, v5
	v_mad_u32_u24 v120, v65, s20, v5
	s_waitcnt vmcnt(13)
	ds_write_b128 v114, v[30:33] offset:64512
	s_waitcnt vmcnt(12)
	ds_write_b128 v115, v[34:37] offset:64512
	s_waitcnt vmcnt(11)
	ds_write_b128 v118, v[38:41] offset:64512
	s_waitcnt vmcnt(10)
	ds_write_b128 v117, v[42:45] offset:64512
	s_waitcnt vmcnt(9)
	ds_write_b128 v119, v[46:49]
	s_waitcnt vmcnt(8)
	ds_write_b128 v120, v[50:53]
	s_waitcnt vmcnt(7)
	ds_write_b128 v119, v[54:57] offset:18432
	v_mad_u64_u32 v[104:105], s[16:17], v6, s20, v[4:5]
	ds_read_b128 v[0:3], v104
	v_mad_u32_u24 v116, v162, s20, v4
	ds_read_b128 v[4:7], v116 offset:36864
	ds_read_b128 v[150:153], v104 offset:32
	ds_read_b128 v[154:157], v116 offset:36896
	ds_read_b128 v[8:11], v116 offset:41472
	ds_read_b128 v[158:161], v116 offset:41504
	ds_read_b128 v[12:15], v116 offset:46080
	ds_read_b128 v[170:173], v116 offset:46112
	s_waitcnt lgkmcnt(0)
	v_mfma_f32_32x32x16_f16 v[80:95], v[0:3], v[4:7], 0
	v_add_u32_e32 v169, 0x1200, v104
	v_mul_u32_u24_e32 v105, 0x90, v162
	v_mfma_f32_32x32x16_f16 v[48:63], v[0:3], v[8:11], 0
	v_mfma_f32_32x32x16_f16 v[16:31], v[0:3], v[12:15], 0
	ds_read_b128 v[0:3], v104 offset:4608
	ds_read_b128 v[174:177], v104 offset:4640
	s_waitcnt lgkmcnt(1)
	v_mfma_f32_32x32x16_f16 v[64:79], v[0:3], v[4:7], 0
	v_mfma_f32_32x32x16_f16 v[32:47], v[0:3], v[8:11], 0
	v_mfma_f32_32x32x16_f16 v[0:15], v[0:3], v[12:15], 0
	v_mfma_f32_32x32x16_f16 v[80:95], v[150:153], v[154:157], v[80:95]
	v_mfma_f32_32x32x16_f16 v[48:63], v[150:153], v[158:161], v[48:63]
	v_mfma_f32_32x32x16_f16 v[16:31], v[150:153], v[170:173], v[16:31]
	s_waitcnt lgkmcnt(0)
	v_mfma_f32_32x32x16_f16 v[64:79], v[174:177], v[154:157], v[64:79]
	v_mfma_f32_32x32x16_f16 v[32:47], v[174:177], v[158:161], v[32:47]
	v_mfma_f32_32x32x16_f16 v[0:15], v[174:177], v[170:173], v[0:15]
	ds_read_b128 v[150:153], v104 offset:64
	ds_read_b128 v[154:157], v116 offset:36928
	ds_read_b128 v[158:161], v104 offset:96
	ds_read_b128 v[170:173], v116 offset:36960
	ds_read_b128 v[174:177], v116 offset:41536
	ds_read_b128 v[178:181], v116 offset:41568
	ds_read_b128 v[182:185], v116 offset:46144
	ds_read_b128 v[186:189], v116 offset:46176
	s_waitcnt lgkmcnt(6)
	v_mfma_f32_32x32x16_f16 v[80:95], v[150:153], v[154:157], v[80:95]
	s_waitcnt lgkmcnt(3)
	v_mfma_f32_32x32x16_f16 v[48:63], v[150:153], v[174:177], v[48:63]
	s_waitcnt lgkmcnt(1)
	v_mfma_f32_32x32x16_f16 v[16:31], v[150:153], v[182:185], v[16:31]
	ds_read_b128 v[150:153], v104 offset:4672
	ds_read_b128 v[190:193], v104 offset:4704
	s_waitcnt lgkmcnt(0)
	s_barrier
	v_mfma_f32_32x32x16_f16 v[64:79], v[150:153], v[154:157], v[64:79]
	v_mfma_f32_32x32x16_f16 v[32:47], v[150:153], v[174:177], v[32:47]
	v_mfma_f32_32x32x16_f16 v[0:15], v[150:153], v[182:185], v[0:15]
	v_mfma_f32_32x32x16_f16 v[80:95], v[158:161], v[170:173], v[80:95]
	v_mfma_f32_32x32x16_f16 v[48:63], v[158:161], v[178:181], v[48:63]
	v_mfma_f32_32x32x16_f16 v[16:31], v[158:161], v[186:189], v[16:31]
	v_mfma_f32_32x32x16_f16 v[64:79], v[190:193], v[170:173], v[64:79]
	v_mfma_f32_32x32x16_f16 v[32:47], v[190:193], v[178:181], v[32:47]
	global_load_dwordx4 v[150:153], v[96:97], off offset:384
	global_load_dwordx4 v[154:157], v[98:99], off offset:384
	global_load_dwordx4 v[158:161], v[100:101], off offset:384
	global_load_dwordx4 v[170:173], v[102:103], off offset:384
	global_load_dwordx4 v[174:177], v[106:107], off offset:384
	global_load_dwordx4 v[178:181], v[108:109], off offset:384
	global_load_dwordx4 v[182:185], v[110:111], off offset:384
	v_mfma_f32_32x32x16_f16 v[0:15], v[190:193], v[186:189], v[0:15]
	s_waitcnt vmcnt(13)
	ds_write_b128 v114, v[122:125]
	s_waitcnt vmcnt(12)
	ds_write_b128 v115, v[126:129]
	s_waitcnt vmcnt(11)
	ds_write_b128 v114, v[130:133] offset:18432
	s_waitcnt vmcnt(10)
	ds_write_b128 v117, v[134:137]
	s_waitcnt vmcnt(9)
	ds_write_b128 v114, v[138:141] offset:36864
	s_waitcnt vmcnt(8)
	ds_write_b128 v115, v[142:145] offset:36864
	s_waitcnt vmcnt(7)
	ds_write_b128 v114, v[146:149] offset:55296
	ds_read_b128 v[122:125], v104 offset:64512
	v_add3_u32 v105, s1, v121, v105
	ds_read_b128 v[126:129], v105
	ds_read_b128 v[130:133], v104 offset:64544
	ds_read_b128 v[134:137], v105 offset:32
	ds_read_b128 v[138:141], v105 offset:4608
	ds_read_b128 v[142:145], v105 offset:4640
	ds_read_b128 v[146:149], v105 offset:9216
	ds_read_b128 v[186:189], v105 offset:9248
	s_waitcnt lgkmcnt(6)
	v_mfma_f32_32x32x16_f16 v[80:95], v[122:125], v[126:129], v[80:95]
	s_waitcnt lgkmcnt(3)
	v_mfma_f32_32x32x16_f16 v[48:63], v[122:125], v[138:141], v[48:63]
	s_waitcnt lgkmcnt(1)
	v_mfma_f32_32x32x16_f16 v[16:31], v[122:125], v[146:149], v[16:31]
	ds_read_b128 v[122:125], v169 offset:64512
	ds_read_b128 v[190:193], v169 offset:64544
	s_waitcnt lgkmcnt(1)
	v_mfma_f32_32x32x16_f16 v[64:79], v[122:125], v[126:129], v[64:79]
	v_mfma_f32_32x32x16_f16 v[32:47], v[122:125], v[138:141], v[32:47]
	v_mfma_f32_32x32x16_f16 v[0:15], v[122:125], v[146:149], v[0:15]
	v_mfma_f32_32x32x16_f16 v[80:95], v[130:133], v[134:137], v[80:95]
	v_mfma_f32_32x32x16_f16 v[48:63], v[130:133], v[142:145], v[48:63]
	v_mfma_f32_32x32x16_f16 v[16:31], v[130:133], v[186:189], v[16:31]
	s_waitcnt lgkmcnt(0)
	v_mfma_f32_32x32x16_f16 v[64:79], v[190:193], v[134:137], v[64:79]
	ds_read_b128 v[122:125], v104 offset:64576
	ds_read_b128 v[126:129], v105 offset:64
	ds_read_b128 v[130:133], v104 offset:64608
	ds_read_b128 v[134:137], v105 offset:96
	v_mfma_f32_32x32x16_f16 v[32:47], v[190:193], v[142:145], v[32:47]
	ds_read_b128 v[138:141], v105 offset:4672
	ds_read_b128 v[142:145], v105 offset:4704
	v_mfma_f32_32x32x16_f16 v[0:15], v[190:193], v[186:189], v[0:15]
	ds_read_b128 v[146:149], v105 offset:9280
	ds_read_b128 v[186:189], v105 offset:9312
	s_waitcnt lgkmcnt(6)
	v_mfma_f32_32x32x16_f16 v[80:95], v[122:125], v[126:129], v[80:95]
	s_waitcnt lgkmcnt(3)
	v_mfma_f32_32x32x16_f16 v[48:63], v[122:125], v[138:141], v[48:63]
	s_waitcnt lgkmcnt(1)
	v_mfma_f32_32x32x16_f16 v[16:31], v[122:125], v[146:149], v[16:31]
	ds_read_b128 v[122:125], v169 offset:64576
	ds_read_b128 v[190:193], v169 offset:64608
	s_waitcnt lgkmcnt(0)
	s_barrier
	v_mfma_f32_32x32x16_f16 v[64:79], v[122:125], v[126:129], v[64:79]
	v_mfma_f32_32x32x16_f16 v[32:47], v[122:125], v[138:141], v[32:47]
	v_mfma_f32_32x32x16_f16 v[0:15], v[122:125], v[146:149], v[0:15]
	v_mfma_f32_32x32x16_f16 v[80:95], v[130:133], v[134:137], v[80:95]
	v_mfma_f32_32x32x16_f16 v[48:63], v[130:133], v[142:145], v[48:63]
	v_mfma_f32_32x32x16_f16 v[16:31], v[130:133], v[186:189], v[16:31]
	v_mfma_f32_32x32x16_f16 v[64:79], v[190:193], v[134:137], v[64:79]
	v_mfma_f32_32x32x16_f16 v[32:47], v[190:193], v[142:145], v[32:47]
	global_load_dwordx4 v[122:125], v[96:97], off offset:512
	global_load_dwordx4 v[126:129], v[98:99], off offset:512
	global_load_dwordx4 v[130:133], v[100:101], off offset:512
	global_load_dwordx4 v[134:137], v[102:103], off offset:512
	global_load_dwordx4 v[138:141], v[106:107], off offset:512
	global_load_dwordx4 v[142:145], v[108:109], off offset:512
	global_load_dwordx4 v[146:149], v[110:111], off offset:512
	v_mfma_f32_32x32x16_f16 v[0:15], v[190:193], v[186:189], v[0:15]
	s_waitcnt vmcnt(13)
	ds_write_b128 v114, v[150:153] offset:64512
	s_waitcnt vmcnt(12)
	ds_write_b128 v115, v[154:157] offset:64512
	s_waitcnt vmcnt(11)
	ds_write_b128 v118, v[158:161] offset:64512
	s_waitcnt vmcnt(10)
	ds_write_b128 v117, v[170:173] offset:64512
	s_waitcnt vmcnt(9)
	ds_write_b128 v119, v[174:177]
	s_waitcnt vmcnt(8)
	ds_write_b128 v120, v[178:181]
	s_waitcnt vmcnt(7)
	ds_write_b128 v119, v[182:185] offset:18432
	ds_read_b128 v[150:153], v104
	ds_read_b128 v[154:157], v116 offset:36864
	ds_read_b128 v[158:161], v104 offset:32
	ds_read_b128 v[170:173], v116 offset:36896
	ds_read_b128 v[174:177], v116 offset:41472
	ds_read_b128 v[178:181], v116 offset:41504
	ds_read_b128 v[182:185], v116 offset:46080
	ds_read_b128 v[186:189], v116 offset:46112
	s_waitcnt lgkmcnt(6)
	v_mfma_f32_32x32x16_f16 v[80:95], v[150:153], v[154:157], v[80:95]
	s_waitcnt lgkmcnt(3)
	v_mfma_f32_32x32x16_f16 v[48:63], v[150:153], v[174:177], v[48:63]
	s_waitcnt lgkmcnt(1)
	v_mfma_f32_32x32x16_f16 v[16:31], v[150:153], v[182:185], v[16:31]
	ds_read_b128 v[150:153], v104 offset:4608
	ds_read_b128 v[190:193], v104 offset:4640
	s_waitcnt lgkmcnt(1)
	v_mfma_f32_32x32x16_f16 v[64:79], v[150:153], v[154:157], v[64:79]
	v_mfma_f32_32x32x16_f16 v[32:47], v[150:153], v[174:177], v[32:47]
	v_mfma_f32_32x32x16_f16 v[0:15], v[150:153], v[182:185], v[0:15]
	v_mfma_f32_32x32x16_f16 v[80:95], v[158:161], v[170:173], v[80:95]
	v_mfma_f32_32x32x16_f16 v[48:63], v[158:161], v[178:181], v[48:63]
	v_mfma_f32_32x32x16_f16 v[16:31], v[158:161], v[186:189], v[16:31]
	s_waitcnt lgkmcnt(0)
	v_mfma_f32_32x32x16_f16 v[64:79], v[190:193], v[170:173], v[64:79]
	ds_read_b128 v[150:153], v104 offset:64
	ds_read_b128 v[154:157], v116 offset:36928
	ds_read_b128 v[158:161], v104 offset:96
	ds_read_b128 v[170:173], v116 offset:36960
	v_mfma_f32_32x32x16_f16 v[32:47], v[190:193], v[178:181], v[32:47]
	ds_read_b128 v[174:177], v116 offset:41536
	ds_read_b128 v[178:181], v116 offset:41568
	v_mfma_f32_32x32x16_f16 v[0:15], v[190:193], v[186:189], v[0:15]
	ds_read_b128 v[182:185], v116 offset:46144
	ds_read_b128 v[186:189], v116 offset:46176
	s_waitcnt lgkmcnt(6)
	v_mfma_f32_32x32x16_f16 v[80:95], v[150:153], v[154:157], v[80:95]
	s_waitcnt lgkmcnt(3)
	v_mfma_f32_32x32x16_f16 v[48:63], v[150:153], v[174:177], v[48:63]
	s_waitcnt lgkmcnt(1)
	v_mfma_f32_32x32x16_f16 v[16:31], v[150:153], v[182:185], v[16:31]
	ds_read_b128 v[150:153], v104 offset:4672
	ds_read_b128 v[190:193], v104 offset:4704
	s_waitcnt lgkmcnt(0)
	s_barrier
	v_mfma_f32_32x32x16_f16 v[64:79], v[150:153], v[154:157], v[64:79]
	v_mfma_f32_32x32x16_f16 v[32:47], v[150:153], v[174:177], v[32:47]
	v_mfma_f32_32x32x16_f16 v[0:15], v[150:153], v[182:185], v[0:15]
	v_mfma_f32_32x32x16_f16 v[80:95], v[158:161], v[170:173], v[80:95]
	v_mfma_f32_32x32x16_f16 v[48:63], v[158:161], v[178:181], v[48:63]
	v_mfma_f32_32x32x16_f16 v[16:31], v[158:161], v[186:189], v[16:31]
	v_mfma_f32_32x32x16_f16 v[64:79], v[190:193], v[170:173], v[64:79]
	v_mfma_f32_32x32x16_f16 v[32:47], v[190:193], v[178:181], v[32:47]
	global_load_dwordx4 v[150:153], v[96:97], off offset:640
	global_load_dwordx4 v[154:157], v[98:99], off offset:640
	global_load_dwordx4 v[158:161], v[100:101], off offset:640
	global_load_dwordx4 v[170:173], v[102:103], off offset:640
	global_load_dwordx4 v[174:177], v[106:107], off offset:640
	global_load_dwordx4 v[178:181], v[108:109], off offset:640
	global_load_dwordx4 v[182:185], v[110:111], off offset:640
	v_mfma_f32_32x32x16_f16 v[0:15], v[190:193], v[186:189], v[0:15]
	s_waitcnt vmcnt(13)
	ds_write_b128 v114, v[122:125]
	s_waitcnt vmcnt(12)
	ds_write_b128 v115, v[126:129]
	s_waitcnt vmcnt(11)
	ds_write_b128 v114, v[130:133] offset:18432
	s_waitcnt vmcnt(10)
	ds_write_b128 v117, v[134:137]
	s_waitcnt vmcnt(9)
	ds_write_b128 v114, v[138:141] offset:36864
	s_waitcnt vmcnt(8)
	ds_write_b128 v115, v[142:145] offset:36864
	s_waitcnt vmcnt(7)
	ds_write_b128 v114, v[146:149] offset:55296
	ds_read_b128 v[122:125], v104 offset:64512
	ds_read_b128 v[126:129], v105
	ds_read_b128 v[130:133], v104 offset:64544
	ds_read_b128 v[134:137], v105 offset:32
	ds_read_b128 v[138:141], v105 offset:4608
	ds_read_b128 v[142:145], v105 offset:4640
	ds_read_b128 v[146:149], v105 offset:9216
	ds_read_b128 v[186:189], v105 offset:9248
	s_waitcnt lgkmcnt(6)
	v_mfma_f32_32x32x16_f16 v[80:95], v[122:125], v[126:129], v[80:95]
	s_waitcnt lgkmcnt(3)
	v_mfma_f32_32x32x16_f16 v[48:63], v[122:125], v[138:141], v[48:63]
	s_waitcnt lgkmcnt(1)
	v_mfma_f32_32x32x16_f16 v[16:31], v[122:125], v[146:149], v[16:31]
	ds_read_b128 v[122:125], v169 offset:64512
	ds_read_b128 v[190:193], v169 offset:64544
	s_waitcnt lgkmcnt(1)
	v_mfma_f32_32x32x16_f16 v[64:79], v[122:125], v[126:129], v[64:79]
	v_mfma_f32_32x32x16_f16 v[32:47], v[122:125], v[138:141], v[32:47]
	v_mfma_f32_32x32x16_f16 v[0:15], v[122:125], v[146:149], v[0:15]
	v_mfma_f32_32x32x16_f16 v[80:95], v[130:133], v[134:137], v[80:95]
	v_mfma_f32_32x32x16_f16 v[48:63], v[130:133], v[142:145], v[48:63]
	v_mfma_f32_32x32x16_f16 v[16:31], v[130:133], v[186:189], v[16:31]
	s_waitcnt lgkmcnt(0)
	v_mfma_f32_32x32x16_f16 v[64:79], v[190:193], v[134:137], v[64:79]
	ds_read_b128 v[122:125], v104 offset:64576
	ds_read_b128 v[126:129], v105 offset:64
	ds_read_b128 v[130:133], v104 offset:64608
	ds_read_b128 v[134:137], v105 offset:96
	v_mfma_f32_32x32x16_f16 v[32:47], v[190:193], v[142:145], v[32:47]
	ds_read_b128 v[138:141], v105 offset:4672
	ds_read_b128 v[142:145], v105 offset:4704
	v_mfma_f32_32x32x16_f16 v[0:15], v[190:193], v[186:189], v[0:15]
	ds_read_b128 v[146:149], v105 offset:9280
	ds_read_b128 v[186:189], v105 offset:9312
	s_waitcnt lgkmcnt(6)
	v_mfma_f32_32x32x16_f16 v[80:95], v[122:125], v[126:129], v[80:95]
	s_waitcnt lgkmcnt(3)
	v_mfma_f32_32x32x16_f16 v[48:63], v[122:125], v[138:141], v[48:63]
	s_waitcnt lgkmcnt(1)
	v_mfma_f32_32x32x16_f16 v[16:31], v[122:125], v[146:149], v[16:31]
	ds_read_b128 v[122:125], v169 offset:64576
	ds_read_b128 v[190:193], v169 offset:64608
	s_waitcnt lgkmcnt(0)
	s_barrier
	v_mfma_f32_32x32x16_f16 v[64:79], v[122:125], v[126:129], v[64:79]
	v_mfma_f32_32x32x16_f16 v[32:47], v[122:125], v[138:141], v[32:47]
	v_mfma_f32_32x32x16_f16 v[0:15], v[122:125], v[146:149], v[0:15]
	v_mfma_f32_32x32x16_f16 v[80:95], v[130:133], v[134:137], v[80:95]
	v_mfma_f32_32x32x16_f16 v[48:63], v[130:133], v[142:145], v[48:63]
	v_mfma_f32_32x32x16_f16 v[16:31], v[130:133], v[186:189], v[16:31]
	v_mfma_f32_32x32x16_f16 v[64:79], v[190:193], v[134:137], v[64:79]
	v_mfma_f32_32x32x16_f16 v[32:47], v[190:193], v[142:145], v[32:47]
	global_load_dwordx4 v[122:125], v[96:97], off offset:768
	global_load_dwordx4 v[126:129], v[98:99], off offset:768
	global_load_dwordx4 v[130:133], v[100:101], off offset:768
	global_load_dwordx4 v[134:137], v[102:103], off offset:768
	global_load_dwordx4 v[138:141], v[106:107], off offset:768
	global_load_dwordx4 v[142:145], v[108:109], off offset:768
	global_load_dwordx4 v[146:149], v[110:111], off offset:768
	v_mfma_f32_32x32x16_f16 v[0:15], v[190:193], v[186:189], v[0:15]
	s_waitcnt vmcnt(13)
	ds_write_b128 v114, v[150:153] offset:64512
	s_waitcnt vmcnt(12)
	ds_write_b128 v115, v[154:157] offset:64512
	s_waitcnt vmcnt(11)
	ds_write_b128 v118, v[158:161] offset:64512
	s_waitcnt vmcnt(10)
	ds_write_b128 v117, v[170:173] offset:64512
	s_waitcnt vmcnt(9)
	ds_write_b128 v119, v[174:177]
	s_waitcnt vmcnt(8)
	ds_write_b128 v120, v[178:181]
	s_waitcnt vmcnt(7)
	ds_write_b128 v119, v[182:185] offset:18432
	ds_read_b128 v[150:153], v104
	ds_read_b128 v[154:157], v116 offset:36864
	ds_read_b128 v[158:161], v104 offset:32
	ds_read_b128 v[170:173], v116 offset:36896
	ds_read_b128 v[174:177], v116 offset:41472
	ds_read_b128 v[178:181], v116 offset:41504
	ds_read_b128 v[182:185], v116 offset:46080
	ds_read_b128 v[186:189], v116 offset:46112
	s_waitcnt lgkmcnt(6)
	v_mfma_f32_32x32x16_f16 v[80:95], v[150:153], v[154:157], v[80:95]
	s_waitcnt lgkmcnt(3)
	v_mfma_f32_32x32x16_f16 v[48:63], v[150:153], v[174:177], v[48:63]
	s_waitcnt lgkmcnt(1)
	v_mfma_f32_32x32x16_f16 v[16:31], v[150:153], v[182:185], v[16:31]
	ds_read_b128 v[150:153], v104 offset:4608
	ds_read_b128 v[190:193], v104 offset:4640
	s_waitcnt lgkmcnt(1)
	v_mfma_f32_32x32x16_f16 v[64:79], v[150:153], v[154:157], v[64:79]
	v_mfma_f32_32x32x16_f16 v[32:47], v[150:153], v[174:177], v[32:47]
	v_mfma_f32_32x32x16_f16 v[0:15], v[150:153], v[182:185], v[0:15]
	v_mfma_f32_32x32x16_f16 v[80:95], v[158:161], v[170:173], v[80:95]
	v_mfma_f32_32x32x16_f16 v[48:63], v[158:161], v[178:181], v[48:63]
	v_mfma_f32_32x32x16_f16 v[16:31], v[158:161], v[186:189], v[16:31]
	s_waitcnt lgkmcnt(0)
	v_mfma_f32_32x32x16_f16 v[64:79], v[190:193], v[170:173], v[64:79]
	ds_read_b128 v[150:153], v104 offset:64
	ds_read_b128 v[154:157], v116 offset:36928
	ds_read_b128 v[158:161], v104 offset:96
	ds_read_b128 v[170:173], v116 offset:36960
	v_mfma_f32_32x32x16_f16 v[32:47], v[190:193], v[178:181], v[32:47]
	ds_read_b128 v[174:177], v116 offset:41536
	ds_read_b128 v[178:181], v116 offset:41568
	v_mfma_f32_32x32x16_f16 v[0:15], v[190:193], v[186:189], v[0:15]
	ds_read_b128 v[182:185], v116 offset:46144
	ds_read_b128 v[186:189], v116 offset:46176
	s_waitcnt lgkmcnt(6)
	v_mfma_f32_32x32x16_f16 v[80:95], v[150:153], v[154:157], v[80:95]
	s_waitcnt lgkmcnt(3)
	v_mfma_f32_32x32x16_f16 v[48:63], v[150:153], v[174:177], v[48:63]
	s_waitcnt lgkmcnt(1)
	v_mfma_f32_32x32x16_f16 v[16:31], v[150:153], v[182:185], v[16:31]
	ds_read_b128 v[150:153], v104 offset:4672
	ds_read_b128 v[190:193], v104 offset:4704
	s_waitcnt lgkmcnt(0)
	s_barrier
	v_mfma_f32_32x32x16_f16 v[64:79], v[150:153], v[154:157], v[64:79]
	v_mfma_f32_32x32x16_f16 v[32:47], v[150:153], v[174:177], v[32:47]
	v_mfma_f32_32x32x16_f16 v[0:15], v[150:153], v[182:185], v[0:15]
	v_mfma_f32_32x32x16_f16 v[80:95], v[158:161], v[170:173], v[80:95]
	v_mfma_f32_32x32x16_f16 v[48:63], v[158:161], v[178:181], v[48:63]
	v_mfma_f32_32x32x16_f16 v[16:31], v[158:161], v[186:189], v[16:31]
	v_mfma_f32_32x32x16_f16 v[64:79], v[190:193], v[170:173], v[64:79]
	v_mfma_f32_32x32x16_f16 v[32:47], v[190:193], v[178:181], v[32:47]
	global_load_dwordx4 v[150:153], v[96:97], off offset:896
	global_load_dwordx4 v[154:157], v[98:99], off offset:896
	global_load_dwordx4 v[158:161], v[100:101], off offset:896
	global_load_dwordx4 v[170:173], v[102:103], off offset:896
	global_load_dwordx4 v[174:177], v[106:107], off offset:896
	global_load_dwordx4 v[178:181], v[108:109], off offset:896
	global_load_dwordx4 v[182:185], v[110:111], off offset:896
	v_mfma_f32_32x32x16_f16 v[0:15], v[190:193], v[186:189], v[0:15]
	s_waitcnt vmcnt(13)
	ds_write_b128 v114, v[122:125]
	s_waitcnt vmcnt(12)
	ds_write_b128 v115, v[126:129]
	s_waitcnt vmcnt(11)
	ds_write_b128 v114, v[130:133] offset:18432
	s_waitcnt vmcnt(10)
	ds_write_b128 v117, v[134:137]
	s_waitcnt vmcnt(9)
	ds_write_b128 v114, v[138:141] offset:36864
	s_waitcnt vmcnt(8)
	ds_write_b128 v115, v[142:145] offset:36864
	s_waitcnt vmcnt(7)
	ds_write_b128 v114, v[146:149] offset:55296
	ds_read_b128 v[122:125], v104 offset:64512
	ds_read_b128 v[126:129], v105
	ds_read_b128 v[130:133], v104 offset:64544
	ds_read_b128 v[134:137], v105 offset:32
	ds_read_b128 v[138:141], v105 offset:4608
	ds_read_b128 v[142:145], v105 offset:4640
	ds_read_b128 v[146:149], v105 offset:9216
	ds_read_b128 v[186:189], v105 offset:9248
	s_waitcnt lgkmcnt(6)
	v_mfma_f32_32x32x16_f16 v[80:95], v[122:125], v[126:129], v[80:95]
	s_waitcnt lgkmcnt(3)
	v_mfma_f32_32x32x16_f16 v[48:63], v[122:125], v[138:141], v[48:63]
	s_waitcnt lgkmcnt(1)
	v_mfma_f32_32x32x16_f16 v[16:31], v[122:125], v[146:149], v[16:31]
	ds_read_b128 v[122:125], v169 offset:64512
	ds_read_b128 v[190:193], v169 offset:64544
	s_waitcnt lgkmcnt(1)
	v_mfma_f32_32x32x16_f16 v[64:79], v[122:125], v[126:129], v[64:79]
	v_mfma_f32_32x32x16_f16 v[32:47], v[122:125], v[138:141], v[32:47]
	v_mfma_f32_32x32x16_f16 v[0:15], v[122:125], v[146:149], v[0:15]
	v_mfma_f32_32x32x16_f16 v[80:95], v[130:133], v[134:137], v[80:95]
	v_mfma_f32_32x32x16_f16 v[48:63], v[130:133], v[142:145], v[48:63]
	v_mfma_f32_32x32x16_f16 v[16:31], v[130:133], v[186:189], v[16:31]
	s_waitcnt lgkmcnt(0)
	v_mfma_f32_32x32x16_f16 v[64:79], v[190:193], v[134:137], v[64:79]
	ds_read_b128 v[122:125], v104 offset:64576
	ds_read_b128 v[126:129], v105 offset:64
	ds_read_b128 v[130:133], v104 offset:64608
	ds_read_b128 v[134:137], v105 offset:96
	v_mfma_f32_32x32x16_f16 v[32:47], v[190:193], v[142:145], v[32:47]
	ds_read_b128 v[138:141], v105 offset:4672
	ds_read_b128 v[142:145], v105 offset:4704
	v_mfma_f32_32x32x16_f16 v[0:15], v[190:193], v[186:189], v[0:15]
	ds_read_b128 v[146:149], v105 offset:9280
	ds_read_b128 v[186:189], v105 offset:9312
	s_waitcnt lgkmcnt(6)
	v_mfma_f32_32x32x16_f16 v[80:95], v[122:125], v[126:129], v[80:95]
	s_waitcnt lgkmcnt(3)
	v_mfma_f32_32x32x16_f16 v[48:63], v[122:125], v[138:141], v[48:63]
	s_waitcnt lgkmcnt(1)
	v_mfma_f32_32x32x16_f16 v[16:31], v[122:125], v[146:149], v[16:31]
	ds_read_b128 v[122:125], v169 offset:64576
	ds_read_b128 v[190:193], v169 offset:64608
	s_waitcnt lgkmcnt(0)
	s_barrier
	v_mfma_f32_32x32x16_f16 v[64:79], v[122:125], v[126:129], v[64:79]
	v_mfma_f32_32x32x16_f16 v[32:47], v[122:125], v[138:141], v[32:47]
	v_mfma_f32_32x32x16_f16 v[0:15], v[122:125], v[146:149], v[0:15]
	v_mfma_f32_32x32x16_f16 v[80:95], v[130:133], v[134:137], v[80:95]
	v_mfma_f32_32x32x16_f16 v[48:63], v[130:133], v[142:145], v[48:63]
	v_mfma_f32_32x32x16_f16 v[16:31], v[130:133], v[186:189], v[16:31]
	v_mfma_f32_32x32x16_f16 v[64:79], v[190:193], v[134:137], v[64:79]
	v_mfma_f32_32x32x16_f16 v[32:47], v[190:193], v[142:145], v[32:47]
	global_load_dwordx4 v[122:125], v[96:97], off offset:1024
	global_load_dwordx4 v[126:129], v[98:99], off offset:1024
	global_load_dwordx4 v[130:133], v[100:101], off offset:1024
	global_load_dwordx4 v[134:137], v[102:103], off offset:1024
	global_load_dwordx4 v[138:141], v[106:107], off offset:1024
	global_load_dwordx4 v[142:145], v[108:109], off offset:1024
	global_load_dwordx4 v[146:149], v[110:111], off offset:1024
	v_mfma_f32_32x32x16_f16 v[0:15], v[190:193], v[186:189], v[0:15]
	s_waitcnt vmcnt(13)
	ds_write_b128 v114, v[150:153] offset:64512
	s_waitcnt vmcnt(12)
	ds_write_b128 v115, v[154:157] offset:64512
	s_waitcnt vmcnt(11)
	ds_write_b128 v118, v[158:161] offset:64512
	s_waitcnt vmcnt(10)
	ds_write_b128 v117, v[170:173] offset:64512
	s_waitcnt vmcnt(9)
	ds_write_b128 v119, v[174:177]
	s_waitcnt vmcnt(8)
	ds_write_b128 v120, v[178:181]
	s_waitcnt vmcnt(7)
	ds_write_b128 v119, v[182:185] offset:18432
	ds_read_b128 v[150:153], v104
	ds_read_b128 v[154:157], v116 offset:36864
	ds_read_b128 v[158:161], v104 offset:32
	ds_read_b128 v[170:173], v116 offset:36896
	ds_read_b128 v[174:177], v116 offset:41472
	ds_read_b128 v[178:181], v116 offset:41504
	ds_read_b128 v[182:185], v116 offset:46080
	ds_read_b128 v[186:189], v116 offset:46112
	s_waitcnt lgkmcnt(6)
	v_mfma_f32_32x32x16_f16 v[80:95], v[150:153], v[154:157], v[80:95]
	s_waitcnt lgkmcnt(3)
	v_mfma_f32_32x32x16_f16 v[48:63], v[150:153], v[174:177], v[48:63]
	s_waitcnt lgkmcnt(1)
	v_mfma_f32_32x32x16_f16 v[16:31], v[150:153], v[182:185], v[16:31]
	ds_read_b128 v[150:153], v104 offset:4608
	ds_read_b128 v[190:193], v104 offset:4640
	s_waitcnt lgkmcnt(1)
	v_mfma_f32_32x32x16_f16 v[64:79], v[150:153], v[154:157], v[64:79]
	v_mfma_f32_32x32x16_f16 v[32:47], v[150:153], v[174:177], v[32:47]
	v_mfma_f32_32x32x16_f16 v[0:15], v[150:153], v[182:185], v[0:15]
	v_mfma_f32_32x32x16_f16 v[80:95], v[158:161], v[170:173], v[80:95]
	v_mfma_f32_32x32x16_f16 v[48:63], v[158:161], v[178:181], v[48:63]
	v_mfma_f32_32x32x16_f16 v[16:31], v[158:161], v[186:189], v[16:31]
	s_waitcnt lgkmcnt(0)
	v_mfma_f32_32x32x16_f16 v[64:79], v[190:193], v[170:173], v[64:79]
	ds_read_b128 v[150:153], v104 offset:64
	ds_read_b128 v[154:157], v116 offset:36928
	ds_read_b128 v[158:161], v104 offset:96
	ds_read_b128 v[170:173], v116 offset:36960
	v_mfma_f32_32x32x16_f16 v[32:47], v[190:193], v[178:181], v[32:47]
	ds_read_b128 v[174:177], v116 offset:41536
	ds_read_b128 v[178:181], v116 offset:41568
	v_mfma_f32_32x32x16_f16 v[0:15], v[190:193], v[186:189], v[0:15]
	ds_read_b128 v[182:185], v116 offset:46144
	ds_read_b128 v[186:189], v116 offset:46176
	s_waitcnt lgkmcnt(6)
	v_mfma_f32_32x32x16_f16 v[80:95], v[150:153], v[154:157], v[80:95]
	s_waitcnt lgkmcnt(3)
	v_mfma_f32_32x32x16_f16 v[48:63], v[150:153], v[174:177], v[48:63]
	s_waitcnt lgkmcnt(1)
	v_mfma_f32_32x32x16_f16 v[16:31], v[150:153], v[182:185], v[16:31]
	ds_read_b128 v[150:153], v104 offset:4672
	ds_read_b128 v[190:193], v104 offset:4704
	s_waitcnt lgkmcnt(0)
	s_barrier
	v_mfma_f32_32x32x16_f16 v[64:79], v[150:153], v[154:157], v[64:79]
	v_mfma_f32_32x32x16_f16 v[32:47], v[150:153], v[174:177], v[32:47]
	v_mfma_f32_32x32x16_f16 v[0:15], v[150:153], v[182:185], v[0:15]
	v_mfma_f32_32x32x16_f16 v[80:95], v[158:161], v[170:173], v[80:95]
	v_mfma_f32_32x32x16_f16 v[48:63], v[158:161], v[178:181], v[48:63]
	v_mfma_f32_32x32x16_f16 v[16:31], v[158:161], v[186:189], v[16:31]
	v_mfma_f32_32x32x16_f16 v[64:79], v[190:193], v[170:173], v[64:79]
	v_mfma_f32_32x32x16_f16 v[32:47], v[190:193], v[178:181], v[32:47]
	global_load_dwordx4 v[150:153], v[96:97], off offset:1152
	global_load_dwordx4 v[154:157], v[98:99], off offset:1152
	global_load_dwordx4 v[158:161], v[100:101], off offset:1152
	global_load_dwordx4 v[170:173], v[102:103], off offset:1152
	global_load_dwordx4 v[174:177], v[106:107], off offset:1152
	global_load_dwordx4 v[178:181], v[108:109], off offset:1152
	global_load_dwordx4 v[182:185], v[110:111], off offset:1152
	v_mfma_f32_32x32x16_f16 v[0:15], v[190:193], v[186:189], v[0:15]
	s_waitcnt vmcnt(13)
	ds_write_b128 v114, v[122:125]
	s_waitcnt vmcnt(12)
	ds_write_b128 v115, v[126:129]
	s_waitcnt vmcnt(11)
	ds_write_b128 v114, v[130:133] offset:18432
	s_waitcnt vmcnt(10)
	ds_write_b128 v117, v[134:137]
	s_waitcnt vmcnt(9)
	ds_write_b128 v114, v[138:141] offset:36864
	s_waitcnt vmcnt(8)
	ds_write_b128 v115, v[142:145] offset:36864
	s_waitcnt vmcnt(7)
	ds_write_b128 v114, v[146:149] offset:55296
	ds_read_b128 v[122:125], v104 offset:64512
	ds_read_b128 v[126:129], v105
	ds_read_b128 v[130:133], v104 offset:64544
	ds_read_b128 v[134:137], v105 offset:32
	ds_read_b128 v[138:141], v105 offset:4608
	ds_read_b128 v[142:145], v105 offset:4640
	ds_read_b128 v[146:149], v105 offset:9216
	ds_read_b128 v[186:189], v105 offset:9248
	s_waitcnt lgkmcnt(6)
	v_mfma_f32_32x32x16_f16 v[80:95], v[122:125], v[126:129], v[80:95]
	s_waitcnt lgkmcnt(3)
	v_mfma_f32_32x32x16_f16 v[48:63], v[122:125], v[138:141], v[48:63]
	s_waitcnt lgkmcnt(1)
	v_mfma_f32_32x32x16_f16 v[16:31], v[122:125], v[146:149], v[16:31]
	ds_read_b128 v[122:125], v169 offset:64512
	ds_read_b128 v[190:193], v169 offset:64544
	s_waitcnt lgkmcnt(1)
	v_mfma_f32_32x32x16_f16 v[64:79], v[122:125], v[126:129], v[64:79]
	v_mfma_f32_32x32x16_f16 v[32:47], v[122:125], v[138:141], v[32:47]
	v_mfma_f32_32x32x16_f16 v[0:15], v[122:125], v[146:149], v[0:15]
	v_mfma_f32_32x32x16_f16 v[80:95], v[130:133], v[134:137], v[80:95]
	v_mfma_f32_32x32x16_f16 v[48:63], v[130:133], v[142:145], v[48:63]
	v_mfma_f32_32x32x16_f16 v[16:31], v[130:133], v[186:189], v[16:31]
	s_waitcnt lgkmcnt(0)
	v_mfma_f32_32x32x16_f16 v[64:79], v[190:193], v[134:137], v[64:79]
	ds_read_b128 v[122:125], v104 offset:64576
	ds_read_b128 v[126:129], v105 offset:64
	ds_read_b128 v[130:133], v104 offset:64608
	ds_read_b128 v[134:137], v105 offset:96
	v_mfma_f32_32x32x16_f16 v[32:47], v[190:193], v[142:145], v[32:47]
	ds_read_b128 v[138:141], v105 offset:4672
	ds_read_b128 v[142:145], v105 offset:4704
	v_mfma_f32_32x32x16_f16 v[0:15], v[190:193], v[186:189], v[0:15]
	ds_read_b128 v[146:149], v105 offset:9280
	ds_read_b128 v[186:189], v105 offset:9312
	s_waitcnt lgkmcnt(6)
	v_mfma_f32_32x32x16_f16 v[80:95], v[122:125], v[126:129], v[80:95]
	s_waitcnt lgkmcnt(3)
	v_mfma_f32_32x32x16_f16 v[48:63], v[122:125], v[138:141], v[48:63]
	s_waitcnt lgkmcnt(1)
	v_mfma_f32_32x32x16_f16 v[16:31], v[122:125], v[146:149], v[16:31]
	ds_read_b128 v[122:125], v169 offset:64576
	ds_read_b128 v[190:193], v169 offset:64608
	s_waitcnt lgkmcnt(0)
	s_barrier
	v_mfma_f32_32x32x16_f16 v[64:79], v[122:125], v[126:129], v[64:79]
	v_mfma_f32_32x32x16_f16 v[32:47], v[122:125], v[138:141], v[32:47]
	v_mfma_f32_32x32x16_f16 v[0:15], v[122:125], v[146:149], v[0:15]
	v_mfma_f32_32x32x16_f16 v[80:95], v[130:133], v[134:137], v[80:95]
	v_mfma_f32_32x32x16_f16 v[48:63], v[130:133], v[142:145], v[48:63]
	v_mfma_f32_32x32x16_f16 v[16:31], v[130:133], v[186:189], v[16:31]
	v_mfma_f32_32x32x16_f16 v[64:79], v[190:193], v[134:137], v[64:79]
	v_mfma_f32_32x32x16_f16 v[32:47], v[190:193], v[142:145], v[32:47]
	global_load_dwordx4 v[122:125], v[96:97], off offset:1280
	global_load_dwordx4 v[126:129], v[98:99], off offset:1280
	global_load_dwordx4 v[130:133], v[100:101], off offset:1280
	global_load_dwordx4 v[134:137], v[102:103], off offset:1280
	global_load_dwordx4 v[138:141], v[106:107], off offset:1280
	global_load_dwordx4 v[142:145], v[108:109], off offset:1280
	global_load_dwordx4 v[146:149], v[110:111], off offset:1280
	v_mfma_f32_32x32x16_f16 v[0:15], v[190:193], v[186:189], v[0:15]
	s_waitcnt vmcnt(13)
	ds_write_b128 v114, v[150:153] offset:64512
	s_waitcnt vmcnt(12)
	ds_write_b128 v115, v[154:157] offset:64512
	s_waitcnt vmcnt(11)
	ds_write_b128 v118, v[158:161] offset:64512
	s_waitcnt vmcnt(10)
	ds_write_b128 v117, v[170:173] offset:64512
	s_waitcnt vmcnt(9)
	ds_write_b128 v119, v[174:177]
	s_waitcnt vmcnt(8)
	ds_write_b128 v120, v[178:181]
	s_waitcnt vmcnt(7)
	ds_write_b128 v119, v[182:185] offset:18432
	ds_read_b128 v[150:153], v104
	ds_read_b128 v[154:157], v116 offset:36864
	ds_read_b128 v[158:161], v104 offset:32
	ds_read_b128 v[170:173], v116 offset:36896
	ds_read_b128 v[174:177], v116 offset:41472
	ds_read_b128 v[178:181], v116 offset:41504
	ds_read_b128 v[182:185], v116 offset:46080
	ds_read_b128 v[186:189], v116 offset:46112
	s_waitcnt lgkmcnt(6)
	v_mfma_f32_32x32x16_f16 v[80:95], v[150:153], v[154:157], v[80:95]
	s_waitcnt lgkmcnt(3)
	v_mfma_f32_32x32x16_f16 v[48:63], v[150:153], v[174:177], v[48:63]
	s_waitcnt lgkmcnt(1)
	v_mfma_f32_32x32x16_f16 v[16:31], v[150:153], v[182:185], v[16:31]
	ds_read_b128 v[150:153], v104 offset:4608
	ds_read_b128 v[190:193], v104 offset:4640
	s_waitcnt lgkmcnt(1)
	v_mfma_f32_32x32x16_f16 v[64:79], v[150:153], v[154:157], v[64:79]
	v_mfma_f32_32x32x16_f16 v[32:47], v[150:153], v[174:177], v[32:47]
	v_mfma_f32_32x32x16_f16 v[0:15], v[150:153], v[182:185], v[0:15]
	v_mfma_f32_32x32x16_f16 v[80:95], v[158:161], v[170:173], v[80:95]
	v_mfma_f32_32x32x16_f16 v[48:63], v[158:161], v[178:181], v[48:63]
	v_mfma_f32_32x32x16_f16 v[16:31], v[158:161], v[186:189], v[16:31]
	s_waitcnt lgkmcnt(0)
	v_mfma_f32_32x32x16_f16 v[64:79], v[190:193], v[170:173], v[64:79]
	ds_read_b128 v[150:153], v104 offset:64
	ds_read_b128 v[154:157], v116 offset:36928
	ds_read_b128 v[158:161], v104 offset:96
	ds_read_b128 v[170:173], v116 offset:36960
	v_mfma_f32_32x32x16_f16 v[32:47], v[190:193], v[178:181], v[32:47]
	ds_read_b128 v[174:177], v116 offset:41536
	ds_read_b128 v[178:181], v116 offset:41568
	v_mfma_f32_32x32x16_f16 v[0:15], v[190:193], v[186:189], v[0:15]
	ds_read_b128 v[182:185], v116 offset:46144
	ds_read_b128 v[186:189], v116 offset:46176
	s_waitcnt lgkmcnt(6)
	v_mfma_f32_32x32x16_f16 v[80:95], v[150:153], v[154:157], v[80:95]
	s_waitcnt lgkmcnt(3)
	v_mfma_f32_32x32x16_f16 v[48:63], v[150:153], v[174:177], v[48:63]
	s_waitcnt lgkmcnt(1)
	v_mfma_f32_32x32x16_f16 v[16:31], v[150:153], v[182:185], v[16:31]
	ds_read_b128 v[150:153], v104 offset:4672
	ds_read_b128 v[190:193], v104 offset:4704
	s_waitcnt lgkmcnt(0)
	s_barrier
	v_mfma_f32_32x32x16_f16 v[64:79], v[150:153], v[154:157], v[64:79]
	v_mfma_f32_32x32x16_f16 v[32:47], v[150:153], v[174:177], v[32:47]
	v_mfma_f32_32x32x16_f16 v[0:15], v[150:153], v[182:185], v[0:15]
	v_mfma_f32_32x32x16_f16 v[80:95], v[158:161], v[170:173], v[80:95]
	v_mfma_f32_32x32x16_f16 v[48:63], v[158:161], v[178:181], v[48:63]
	v_mfma_f32_32x32x16_f16 v[16:31], v[158:161], v[186:189], v[16:31]
	v_mfma_f32_32x32x16_f16 v[64:79], v[190:193], v[170:173], v[64:79]
	v_mfma_f32_32x32x16_f16 v[32:47], v[190:193], v[178:181], v[32:47]
	global_load_dwordx4 v[150:153], v[96:97], off offset:1408
	global_load_dwordx4 v[154:157], v[98:99], off offset:1408
	global_load_dwordx4 v[158:161], v[100:101], off offset:1408
	global_load_dwordx4 v[170:173], v[102:103], off offset:1408
	global_load_dwordx4 v[174:177], v[106:107], off offset:1408
	global_load_dwordx4 v[178:181], v[108:109], off offset:1408
	global_load_dwordx4 v[182:185], v[110:111], off offset:1408
	v_mfma_f32_32x32x16_f16 v[0:15], v[190:193], v[186:189], v[0:15]
	s_waitcnt vmcnt(13)
	ds_write_b128 v114, v[122:125]
	s_waitcnt vmcnt(12)
	ds_write_b128 v115, v[126:129]
	s_waitcnt vmcnt(11)
	ds_write_b128 v114, v[130:133] offset:18432
	s_waitcnt vmcnt(10)
	ds_write_b128 v117, v[134:137]
	s_waitcnt vmcnt(9)
	ds_write_b128 v114, v[138:141] offset:36864
	s_waitcnt vmcnt(8)
	ds_write_b128 v115, v[142:145] offset:36864
	s_waitcnt vmcnt(7)
	ds_write_b128 v114, v[146:149] offset:55296
	ds_read_b128 v[122:125], v104 offset:64512
	ds_read_b128 v[126:129], v105
	ds_read_b128 v[130:133], v104 offset:64544
	ds_read_b128 v[134:137], v105 offset:32
	ds_read_b128 v[138:141], v105 offset:4608
	ds_read_b128 v[142:145], v105 offset:4640
	ds_read_b128 v[146:149], v105 offset:9216
	ds_read_b128 v[186:189], v105 offset:9248
	s_waitcnt lgkmcnt(6)
	v_mfma_f32_32x32x16_f16 v[80:95], v[122:125], v[126:129], v[80:95]
	s_waitcnt lgkmcnt(3)
	v_mfma_f32_32x32x16_f16 v[48:63], v[122:125], v[138:141], v[48:63]
	s_waitcnt lgkmcnt(1)
	v_mfma_f32_32x32x16_f16 v[16:31], v[122:125], v[146:149], v[16:31]
	ds_read_b128 v[122:125], v169 offset:64512
	ds_read_b128 v[190:193], v169 offset:64544
	s_waitcnt lgkmcnt(1)
	v_mfma_f32_32x32x16_f16 v[64:79], v[122:125], v[126:129], v[64:79]
	v_mfma_f32_32x32x16_f16 v[32:47], v[122:125], v[138:141], v[32:47]
	v_mfma_f32_32x32x16_f16 v[0:15], v[122:125], v[146:149], v[0:15]
	v_mfma_f32_32x32x16_f16 v[80:95], v[130:133], v[134:137], v[80:95]
	v_mfma_f32_32x32x16_f16 v[48:63], v[130:133], v[142:145], v[48:63]
	v_mfma_f32_32x32x16_f16 v[16:31], v[130:133], v[186:189], v[16:31]
	s_waitcnt lgkmcnt(0)
	v_mfma_f32_32x32x16_f16 v[64:79], v[190:193], v[134:137], v[64:79]
	ds_read_b128 v[122:125], v104 offset:64576
	ds_read_b128 v[126:129], v105 offset:64
	ds_read_b128 v[130:133], v104 offset:64608
	ds_read_b128 v[134:137], v105 offset:96
	v_mfma_f32_32x32x16_f16 v[32:47], v[190:193], v[142:145], v[32:47]
	ds_read_b128 v[138:141], v105 offset:4672
	ds_read_b128 v[142:145], v105 offset:4704
	v_mfma_f32_32x32x16_f16 v[0:15], v[190:193], v[186:189], v[0:15]
	ds_read_b128 v[146:149], v105 offset:9280
	ds_read_b128 v[186:189], v105 offset:9312
	s_waitcnt lgkmcnt(6)
	v_mfma_f32_32x32x16_f16 v[80:95], v[122:125], v[126:129], v[80:95]
	s_waitcnt lgkmcnt(3)
	v_mfma_f32_32x32x16_f16 v[48:63], v[122:125], v[138:141], v[48:63]
	s_waitcnt lgkmcnt(1)
	v_mfma_f32_32x32x16_f16 v[16:31], v[122:125], v[146:149], v[16:31]
	ds_read_b128 v[122:125], v169 offset:64576
	ds_read_b128 v[190:193], v169 offset:64608
	s_waitcnt lgkmcnt(0)
	s_barrier
	v_mfma_f32_32x32x16_f16 v[64:79], v[122:125], v[126:129], v[64:79]
	v_mfma_f32_32x32x16_f16 v[32:47], v[122:125], v[138:141], v[32:47]
	v_mfma_f32_32x32x16_f16 v[0:15], v[122:125], v[146:149], v[0:15]
	v_mfma_f32_32x32x16_f16 v[80:95], v[130:133], v[134:137], v[80:95]
	v_mfma_f32_32x32x16_f16 v[48:63], v[130:133], v[142:145], v[48:63]
	v_mfma_f32_32x32x16_f16 v[16:31], v[130:133], v[186:189], v[16:31]
	v_mfma_f32_32x32x16_f16 v[64:79], v[190:193], v[134:137], v[64:79]
	v_mfma_f32_32x32x16_f16 v[32:47], v[190:193], v[142:145], v[32:47]
	global_load_dwordx4 v[122:125], v[96:97], off offset:1536
	global_load_dwordx4 v[126:129], v[98:99], off offset:1536
	global_load_dwordx4 v[130:133], v[100:101], off offset:1536
	global_load_dwordx4 v[134:137], v[102:103], off offset:1536
	global_load_dwordx4 v[138:141], v[106:107], off offset:1536
	global_load_dwordx4 v[142:145], v[108:109], off offset:1536
	global_load_dwordx4 v[146:149], v[110:111], off offset:1536
	v_mfma_f32_32x32x16_f16 v[0:15], v[190:193], v[186:189], v[0:15]
	s_waitcnt vmcnt(13)
	ds_write_b128 v114, v[150:153] offset:64512
	s_waitcnt vmcnt(12)
	ds_write_b128 v115, v[154:157] offset:64512
	s_waitcnt vmcnt(11)
	ds_write_b128 v118, v[158:161] offset:64512
	s_waitcnt vmcnt(10)
	ds_write_b128 v117, v[170:173] offset:64512
	s_waitcnt vmcnt(9)
	ds_write_b128 v119, v[174:177]
	s_waitcnt vmcnt(8)
	ds_write_b128 v120, v[178:181]
	s_waitcnt vmcnt(7)
	ds_write_b128 v119, v[182:185] offset:18432
	ds_read_b128 v[150:153], v104
	ds_read_b128 v[154:157], v116 offset:36864
	ds_read_b128 v[158:161], v104 offset:32
	ds_read_b128 v[170:173], v116 offset:36896
	ds_read_b128 v[174:177], v116 offset:41472
	ds_read_b128 v[178:181], v116 offset:41504
	ds_read_b128 v[182:185], v116 offset:46080
	ds_read_b128 v[186:189], v116 offset:46112
	s_waitcnt lgkmcnt(6)
	v_mfma_f32_32x32x16_f16 v[80:95], v[150:153], v[154:157], v[80:95]
	s_waitcnt lgkmcnt(3)
	v_mfma_f32_32x32x16_f16 v[48:63], v[150:153], v[174:177], v[48:63]
	s_waitcnt lgkmcnt(1)
	v_mfma_f32_32x32x16_f16 v[16:31], v[150:153], v[182:185], v[16:31]
	ds_read_b128 v[150:153], v104 offset:4608
	ds_read_b128 v[190:193], v104 offset:4640
	s_waitcnt lgkmcnt(1)
	v_mfma_f32_32x32x16_f16 v[64:79], v[150:153], v[154:157], v[64:79]
	v_mfma_f32_32x32x16_f16 v[32:47], v[150:153], v[174:177], v[32:47]
	v_mfma_f32_32x32x16_f16 v[0:15], v[150:153], v[182:185], v[0:15]
	v_mfma_f32_32x32x16_f16 v[80:95], v[158:161], v[170:173], v[80:95]
	v_mfma_f32_32x32x16_f16 v[48:63], v[158:161], v[178:181], v[48:63]
	v_mfma_f32_32x32x16_f16 v[16:31], v[158:161], v[186:189], v[16:31]
	s_waitcnt lgkmcnt(0)
	v_mfma_f32_32x32x16_f16 v[64:79], v[190:193], v[170:173], v[64:79]
	ds_read_b128 v[150:153], v104 offset:64
	ds_read_b128 v[154:157], v116 offset:36928
	ds_read_b128 v[158:161], v104 offset:96
	ds_read_b128 v[170:173], v116 offset:36960
	v_mfma_f32_32x32x16_f16 v[32:47], v[190:193], v[178:181], v[32:47]
	ds_read_b128 v[174:177], v116 offset:41536
	ds_read_b128 v[178:181], v116 offset:41568
	v_mfma_f32_32x32x16_f16 v[0:15], v[190:193], v[186:189], v[0:15]
	ds_read_b128 v[182:185], v116 offset:46144
	ds_read_b128 v[186:189], v116 offset:46176
	s_waitcnt lgkmcnt(6)
	v_mfma_f32_32x32x16_f16 v[80:95], v[150:153], v[154:157], v[80:95]
	s_waitcnt lgkmcnt(3)
	v_mfma_f32_32x32x16_f16 v[48:63], v[150:153], v[174:177], v[48:63]
	s_waitcnt lgkmcnt(1)
	v_mfma_f32_32x32x16_f16 v[16:31], v[150:153], v[182:185], v[16:31]
	ds_read_b128 v[150:153], v104 offset:4672
	ds_read_b128 v[190:193], v104 offset:4704
	s_waitcnt lgkmcnt(0)
	s_barrier
	v_mfma_f32_32x32x16_f16 v[64:79], v[150:153], v[154:157], v[64:79]
	v_mfma_f32_32x32x16_f16 v[32:47], v[150:153], v[174:177], v[32:47]
	v_mfma_f32_32x32x16_f16 v[0:15], v[150:153], v[182:185], v[0:15]
	v_mfma_f32_32x32x16_f16 v[80:95], v[158:161], v[170:173], v[80:95]
	v_mfma_f32_32x32x16_f16 v[48:63], v[158:161], v[178:181], v[48:63]
	v_mfma_f32_32x32x16_f16 v[16:31], v[158:161], v[186:189], v[16:31]
	v_mfma_f32_32x32x16_f16 v[64:79], v[190:193], v[170:173], v[64:79]
	v_mfma_f32_32x32x16_f16 v[32:47], v[190:193], v[178:181], v[32:47]
	global_load_dwordx4 v[150:153], v[96:97], off offset:1664
	global_load_dwordx4 v[154:157], v[98:99], off offset:1664
	global_load_dwordx4 v[158:161], v[100:101], off offset:1664
	global_load_dwordx4 v[170:173], v[102:103], off offset:1664
	global_load_dwordx4 v[174:177], v[106:107], off offset:1664
	global_load_dwordx4 v[178:181], v[108:109], off offset:1664
	global_load_dwordx4 v[182:185], v[110:111], off offset:1664
	v_mfma_f32_32x32x16_f16 v[0:15], v[190:193], v[186:189], v[0:15]
	s_waitcnt vmcnt(13)
	ds_write_b128 v114, v[122:125]
	s_waitcnt vmcnt(12)
	ds_write_b128 v115, v[126:129]
	s_waitcnt vmcnt(11)
	ds_write_b128 v114, v[130:133] offset:18432
	s_waitcnt vmcnt(10)
	ds_write_b128 v117, v[134:137]
	s_waitcnt vmcnt(9)
	ds_write_b128 v114, v[138:141] offset:36864
	s_waitcnt vmcnt(8)
	ds_write_b128 v115, v[142:145] offset:36864
	s_waitcnt vmcnt(7)
	ds_write_b128 v114, v[146:149] offset:55296
	ds_read_b128 v[122:125], v104 offset:64512
	ds_read_b128 v[126:129], v105
	ds_read_b128 v[130:133], v104 offset:64544
	ds_read_b128 v[134:137], v105 offset:32
	ds_read_b128 v[138:141], v105 offset:4608
	ds_read_b128 v[142:145], v105 offset:4640
	ds_read_b128 v[146:149], v105 offset:9216
	ds_read_b128 v[186:189], v105 offset:9248
	s_waitcnt lgkmcnt(6)
	v_mfma_f32_32x32x16_f16 v[80:95], v[122:125], v[126:129], v[80:95]
	s_waitcnt lgkmcnt(3)
	v_mfma_f32_32x32x16_f16 v[48:63], v[122:125], v[138:141], v[48:63]
	s_waitcnt lgkmcnt(1)
	v_mfma_f32_32x32x16_f16 v[16:31], v[122:125], v[146:149], v[16:31]
	ds_read_b128 v[122:125], v169 offset:64512
	ds_read_b128 v[190:193], v169 offset:64544
	s_waitcnt lgkmcnt(1)
	v_mfma_f32_32x32x16_f16 v[64:79], v[122:125], v[126:129], v[64:79]
	v_mfma_f32_32x32x16_f16 v[32:47], v[122:125], v[138:141], v[32:47]
	v_mfma_f32_32x32x16_f16 v[0:15], v[122:125], v[146:149], v[0:15]
	v_mfma_f32_32x32x16_f16 v[80:95], v[130:133], v[134:137], v[80:95]
	v_mfma_f32_32x32x16_f16 v[48:63], v[130:133], v[142:145], v[48:63]
	v_mfma_f32_32x32x16_f16 v[16:31], v[130:133], v[186:189], v[16:31]
	s_waitcnt lgkmcnt(0)
	v_mfma_f32_32x32x16_f16 v[64:79], v[190:193], v[134:137], v[64:79]
	ds_read_b128 v[122:125], v104 offset:64576
	ds_read_b128 v[126:129], v105 offset:64
	ds_read_b128 v[130:133], v104 offset:64608
	ds_read_b128 v[134:137], v105 offset:96
	v_mfma_f32_32x32x16_f16 v[32:47], v[190:193], v[142:145], v[32:47]
	ds_read_b128 v[138:141], v105 offset:4672
	ds_read_b128 v[142:145], v105 offset:4704
	v_mfma_f32_32x32x16_f16 v[0:15], v[190:193], v[186:189], v[0:15]
	ds_read_b128 v[146:149], v105 offset:9280
	ds_read_b128 v[186:189], v105 offset:9312
	s_waitcnt lgkmcnt(6)
	v_mfma_f32_32x32x16_f16 v[80:95], v[122:125], v[126:129], v[80:95]
	s_waitcnt lgkmcnt(3)
	v_mfma_f32_32x32x16_f16 v[48:63], v[122:125], v[138:141], v[48:63]
	s_waitcnt lgkmcnt(1)
	v_mfma_f32_32x32x16_f16 v[16:31], v[122:125], v[146:149], v[16:31]
	ds_read_b128 v[122:125], v169 offset:64576
	ds_read_b128 v[190:193], v169 offset:64608
	s_waitcnt lgkmcnt(0)
	s_barrier
	v_mfma_f32_32x32x16_f16 v[64:79], v[122:125], v[126:129], v[64:79]
	v_mfma_f32_32x32x16_f16 v[32:47], v[122:125], v[138:141], v[32:47]
	v_mfma_f32_32x32x16_f16 v[0:15], v[122:125], v[146:149], v[0:15]
	v_mfma_f32_32x32x16_f16 v[80:95], v[130:133], v[134:137], v[80:95]
	v_mfma_f32_32x32x16_f16 v[48:63], v[130:133], v[142:145], v[48:63]
	v_mfma_f32_32x32x16_f16 v[16:31], v[130:133], v[186:189], v[16:31]
	v_mfma_f32_32x32x16_f16 v[64:79], v[190:193], v[134:137], v[64:79]
	v_mfma_f32_32x32x16_f16 v[32:47], v[190:193], v[142:145], v[32:47]
	global_load_dwordx4 v[122:125], v[96:97], off offset:1792
	global_load_dwordx4 v[126:129], v[98:99], off offset:1792
	global_load_dwordx4 v[130:133], v[100:101], off offset:1792
	global_load_dwordx4 v[134:137], v[102:103], off offset:1792
	global_load_dwordx4 v[138:141], v[106:107], off offset:1792
	global_load_dwordx4 v[142:145], v[108:109], off offset:1792
	global_load_dwordx4 v[146:149], v[110:111], off offset:1792
	v_mfma_f32_32x32x16_f16 v[0:15], v[190:193], v[186:189], v[0:15]
	s_waitcnt vmcnt(13)
	ds_write_b128 v114, v[150:153] offset:64512
	s_waitcnt vmcnt(12)
	ds_write_b128 v115, v[154:157] offset:64512
	s_waitcnt vmcnt(11)
	ds_write_b128 v118, v[158:161] offset:64512
	s_waitcnt vmcnt(10)
	ds_write_b128 v117, v[170:173] offset:64512
	s_waitcnt vmcnt(9)
	ds_write_b128 v119, v[174:177]
	s_waitcnt vmcnt(8)
	ds_write_b128 v120, v[178:181]
	s_waitcnt vmcnt(7)
	ds_write_b128 v119, v[182:185] offset:18432
	ds_read_b128 v[150:153], v104
	ds_read_b128 v[154:157], v116 offset:36864
	ds_read_b128 v[158:161], v104 offset:32
	ds_read_b128 v[170:173], v116 offset:36896
	ds_read_b128 v[174:177], v116 offset:41472
	ds_read_b128 v[178:181], v116 offset:41504
	ds_read_b128 v[182:185], v116 offset:46080
	ds_read_b128 v[186:189], v116 offset:46112
	s_waitcnt lgkmcnt(6)
	v_mfma_f32_32x32x16_f16 v[80:95], v[150:153], v[154:157], v[80:95]
	s_waitcnt lgkmcnt(3)
	v_mfma_f32_32x32x16_f16 v[48:63], v[150:153], v[174:177], v[48:63]
	s_waitcnt lgkmcnt(1)
	v_mfma_f32_32x32x16_f16 v[16:31], v[150:153], v[182:185], v[16:31]
	ds_read_b128 v[150:153], v104 offset:4608
	ds_read_b128 v[190:193], v104 offset:4640
	s_waitcnt lgkmcnt(1)
	v_mfma_f32_32x32x16_f16 v[64:79], v[150:153], v[154:157], v[64:79]
	v_mfma_f32_32x32x16_f16 v[32:47], v[150:153], v[174:177], v[32:47]
	v_mfma_f32_32x32x16_f16 v[0:15], v[150:153], v[182:185], v[0:15]
	v_mfma_f32_32x32x16_f16 v[80:95], v[158:161], v[170:173], v[80:95]
	v_mfma_f32_32x32x16_f16 v[48:63], v[158:161], v[178:181], v[48:63]
	v_mfma_f32_32x32x16_f16 v[16:31], v[158:161], v[186:189], v[16:31]
	s_waitcnt lgkmcnt(0)
	v_mfma_f32_32x32x16_f16 v[64:79], v[190:193], v[170:173], v[64:79]
	ds_read_b128 v[150:153], v104 offset:64
	ds_read_b128 v[154:157], v116 offset:36928
	ds_read_b128 v[158:161], v104 offset:96
	ds_read_b128 v[170:173], v116 offset:36960
	v_mfma_f32_32x32x16_f16 v[32:47], v[190:193], v[178:181], v[32:47]
	ds_read_b128 v[174:177], v116 offset:41536
	ds_read_b128 v[178:181], v116 offset:41568
	v_mfma_f32_32x32x16_f16 v[0:15], v[190:193], v[186:189], v[0:15]
	ds_read_b128 v[182:185], v116 offset:46144
	ds_read_b128 v[186:189], v116 offset:46176
	s_waitcnt lgkmcnt(6)
	v_mfma_f32_32x32x16_f16 v[80:95], v[150:153], v[154:157], v[80:95]
	s_waitcnt lgkmcnt(3)
	v_mfma_f32_32x32x16_f16 v[48:63], v[150:153], v[174:177], v[48:63]
	s_waitcnt lgkmcnt(1)
	v_mfma_f32_32x32x16_f16 v[16:31], v[150:153], v[182:185], v[16:31]
	ds_read_b128 v[150:153], v104 offset:4672
	ds_read_b128 v[190:193], v104 offset:4704
	s_waitcnt lgkmcnt(0)
	s_barrier
	v_mfma_f32_32x32x16_f16 v[64:79], v[150:153], v[154:157], v[64:79]
	v_mfma_f32_32x32x16_f16 v[32:47], v[150:153], v[174:177], v[32:47]
	v_mfma_f32_32x32x16_f16 v[0:15], v[150:153], v[182:185], v[0:15]
	v_mfma_f32_32x32x16_f16 v[80:95], v[158:161], v[170:173], v[80:95]
	v_mfma_f32_32x32x16_f16 v[48:63], v[158:161], v[178:181], v[48:63]
	v_mfma_f32_32x32x16_f16 v[16:31], v[158:161], v[186:189], v[16:31]
	v_mfma_f32_32x32x16_f16 v[64:79], v[190:193], v[170:173], v[64:79]
	global_load_dwordx4 v[150:153], v[96:97], off offset:1920
	s_nop 0
	global_load_dwordx4 v[96:99], v[98:99], off offset:1920
	s_nop 0
	global_load_dwordx4 v[154:157], v[100:101], off offset:1920
	s_nop 0
	global_load_dwordx4 v[100:103], v[102:103], off offset:1920
	s_nop 0
	global_load_dwordx4 v[158:161], v[106:107], off offset:1920
	s_nop 0
	global_load_dwordx4 v[106:109], v[108:109], off offset:1920
	s_nop 0
	global_load_dwordx4 v[170:173], v[110:111], off offset:1920
	v_mfma_f32_32x32x16_f16 v[32:47], v[190:193], v[178:181], v[32:47]
	v_mfma_f32_32x32x16_f16 v[0:15], v[190:193], v[186:189], v[0:15]
	s_waitcnt vmcnt(13)
	ds_write_b128 v114, v[122:125]
	s_waitcnt vmcnt(12)
	ds_write_b128 v115, v[126:129]
	s_waitcnt vmcnt(11)
	ds_write_b128 v114, v[130:133] offset:18432
	s_waitcnt vmcnt(10)
	ds_write_b128 v117, v[134:137]
	s_waitcnt vmcnt(9)
	ds_write_b128 v114, v[138:141] offset:36864
	s_waitcnt vmcnt(8)
	ds_write_b128 v115, v[142:145] offset:36864
	s_waitcnt vmcnt(7)
	ds_write_b128 v114, v[146:149] offset:55296
	ds_read_b128 v[122:125], v104 offset:64512
	ds_read_b128 v[126:129], v105
	ds_read_b128 v[130:133], v104 offset:64544
	ds_read_b128 v[134:137], v105 offset:32
	ds_read_b128 v[138:141], v105 offset:4608
	ds_read_b128 v[142:145], v105 offset:4640
	ds_read_b128 v[146:149], v105 offset:9216
	ds_read_b128 v[174:177], v105 offset:9248
	s_waitcnt lgkmcnt(6)
	v_mfma_f32_32x32x16_f16 v[80:95], v[122:125], v[126:129], v[80:95]
	s_waitcnt lgkmcnt(3)
	v_mfma_f32_32x32x16_f16 v[48:63], v[122:125], v[138:141], v[48:63]
	s_waitcnt lgkmcnt(1)
	v_mfma_f32_32x32x16_f16 v[16:31], v[122:125], v[146:149], v[16:31]
	ds_read_b128 v[122:125], v169 offset:64512
	ds_read_b128 v[178:181], v169 offset:64544
	s_waitcnt lgkmcnt(1)
	v_mfma_f32_32x32x16_f16 v[64:79], v[122:125], v[126:129], v[64:79]
	v_mfma_f32_32x32x16_f16 v[32:47], v[122:125], v[138:141], v[32:47]
	v_mfma_f32_32x32x16_f16 v[0:15], v[122:125], v[146:149], v[0:15]
	v_mfma_f32_32x32x16_f16 v[80:95], v[130:133], v[134:137], v[80:95]
	v_mfma_f32_32x32x16_f16 v[48:63], v[130:133], v[142:145], v[48:63]
	v_mfma_f32_32x32x16_f16 v[16:31], v[130:133], v[174:177], v[16:31]
	s_waitcnt lgkmcnt(0)
	v_mfma_f32_32x32x16_f16 v[64:79], v[178:181], v[134:137], v[64:79]
	ds_read_b128 v[122:125], v104 offset:64576
	ds_read_b128 v[126:129], v105 offset:64
	ds_read_b128 v[130:133], v104 offset:64608
	ds_read_b128 v[134:137], v105 offset:96
	v_mfma_f32_32x32x16_f16 v[32:47], v[178:181], v[142:145], v[32:47]
	ds_read_b128 v[138:141], v105 offset:4672
	ds_read_b128 v[142:145], v105 offset:4704
	v_mfma_f32_32x32x16_f16 v[0:15], v[178:181], v[174:177], v[0:15]
	ds_read_b128 v[146:149], v105 offset:9280
	ds_read_b128 v[174:177], v105 offset:9312
	s_waitcnt lgkmcnt(6)
	v_mfma_f32_32x32x16_f16 v[80:95], v[122:125], v[126:129], v[80:95]
	s_waitcnt lgkmcnt(3)
	v_mfma_f32_32x32x16_f16 v[48:63], v[122:125], v[138:141], v[48:63]
	s_waitcnt lgkmcnt(1)
	v_mfma_f32_32x32x16_f16 v[16:31], v[122:125], v[146:149], v[16:31]
	ds_read_b128 v[122:125], v169 offset:64576
	ds_read_b128 v[178:181], v169 offset:64608
	s_waitcnt lgkmcnt(0)
	s_barrier
	v_mfma_f32_32x32x16_f16 v[64:79], v[122:125], v[126:129], v[64:79]
	v_mfma_f32_32x32x16_f16 v[32:47], v[122:125], v[138:141], v[32:47]
	v_mfma_f32_32x32x16_f16 v[0:15], v[122:125], v[146:149], v[0:15]
	v_mfma_f32_32x32x16_f16 v[80:95], v[130:133], v[134:137], v[80:95]
	v_mfma_f32_32x32x16_f16 v[48:63], v[130:133], v[142:145], v[48:63]
	v_mfma_f32_32x32x16_f16 v[16:31], v[130:133], v[174:177], v[16:31]
	v_mfma_f32_32x32x16_f16 v[64:79], v[178:181], v[134:137], v[64:79]
	v_mfma_f32_32x32x16_f16 v[32:47], v[178:181], v[142:145], v[32:47]
	v_mfma_f32_32x32x16_f16 v[0:15], v[178:181], v[174:177], v[0:15]
	s_waitcnt vmcnt(6)
	ds_write_b128 v114, v[150:153] offset:64512
	s_waitcnt vmcnt(5)
	ds_write_b128 v115, v[96:99] offset:64512
	s_waitcnt vmcnt(4)
	ds_write_b128 v118, v[154:157] offset:64512
	s_waitcnt vmcnt(3)
	ds_write_b128 v117, v[100:103] offset:64512
	s_waitcnt vmcnt(2)
	ds_write_b128 v119, v[158:161]
	s_waitcnt vmcnt(1)
	ds_write_b128 v120, v[106:109]
	s_waitcnt vmcnt(0)
	ds_write_b128 v119, v[170:173] offset:18432
	ds_read_b128 v[96:99], v104
	ds_read_b128 v[100:103], v116 offset:36864
	ds_read_b128 v[106:109], v104 offset:32
	ds_read_b128 v[118:121], v116 offset:36896
	ds_read_b128 v[122:125], v116 offset:41472
	ds_read_b128 v[126:129], v116 offset:41504
	ds_read_b128 v[130:133], v116 offset:46080
	ds_read_b128 v[134:137], v116 offset:46112
	s_waitcnt lgkmcnt(6)
	v_mfma_f32_32x32x16_f16 v[80:95], v[96:99], v[100:103], v[80:95]
	s_waitcnt lgkmcnt(3)
	v_mfma_f32_32x32x16_f16 v[48:63], v[96:99], v[122:125], v[48:63]
	s_waitcnt lgkmcnt(1)
	v_mfma_f32_32x32x16_f16 v[16:31], v[96:99], v[130:133], v[16:31]
	ds_read_b128 v[96:99], v104 offset:4608
	ds_read_b128 v[138:141], v104 offset:4640
	v_mfma_f32_32x32x16_f16 v[80:95], v[106:109], v[118:121], v[80:95]
	v_mfma_f32_32x32x16_f16 v[48:63], v[106:109], v[126:129], v[48:63]
	s_waitcnt lgkmcnt(2)
	v_mfma_f32_32x32x16_f16 v[16:31], v[106:109], v[134:137], v[16:31]
	v_lshlrev_b32_e32 v106, 5, v167
	v_and_b32_e32 v106, 0xf8a0, v106
	v_or_b32_e32 v107, v106, v113
	v_or_b32_e32 v108, v106, v112
	v_lshlrev_b32_e32 v107, 2, v107
	v_lshlrev_b32_e32 v108, 2, v108
	s_waitcnt lgkmcnt(1)
	v_mfma_f32_32x32x16_f16 v[64:79], v[96:99], v[100:103], v[64:79]
	v_mfma_f32_32x32x16_f16 v[32:47], v[96:99], v[122:125], v[32:47]
	v_mfma_f32_32x32x16_f16 v[0:15], v[96:99], v[130:133], v[0:15]
	ds_read_b128 v[96:99], v104 offset:64
	ds_read_b128 v[100:103], v104 offset:96
	ds_read_b128 v[122:125], v104 offset:4672
	ds_read_b128 v[130:133], v104 offset:4704
	ds_read_b128 v[142:145], v116 offset:36928
	ds_read_b128 v[146:149], v116 offset:36960
	ds_read_b128 v[150:153], v116 offset:41536
	ds_read_b128 v[154:157], v116 offset:41568
	ds_read_b128 v[158:161], v116 offset:46144
	ds_read_b128 v[114:117], v116 offset:46176
	s_waitcnt lgkmcnt(0)
	s_barrier
	global_load_dword v200, v107, s[8:9]
	global_load_dword v201, v107, s[10:11]
	global_load_dword v198, v107, s[8:9] offset:256
	global_load_dword v199, v107, s[10:11] offset:256
	global_load_dword v196, v107, s[8:9] offset:1024
	global_load_dword v197, v107, s[10:11] offset:1024
	global_load_dword v194, v107, s[8:9] offset:1280
	global_load_dword v195, v107, s[10:11] offset:1280
	global_load_dword v233, v108, s[8:9]
	global_load_dword v234, v108, s[10:11]
	global_load_dword v231, v108, s[8:9] offset:256
	global_load_dword v232, v108, s[10:11] offset:256
	global_load_dword v229, v108, s[8:9] offset:1024
	global_load_dword v230, v108, s[10:11] offset:1024
	global_load_dword v226, v108, s[8:9] offset:1280
	global_load_dword v227, v108, s[10:11] offset:1280
	global_load_dword v192, v107, s[8:9] offset:2048
	global_load_dword v193, v107, s[10:11] offset:2048
	global_load_dword v190, v107, s[8:9] offset:2304
	global_load_dword v191, v107, s[10:11] offset:2304
	global_load_dword v188, v107, s[8:9] offset:3072
	global_load_dword v189, v107, s[10:11] offset:3072
	global_load_dword v186, v107, s[8:9] offset:3328
	global_load_dword v187, v107, s[10:11] offset:3328
	v_mfma_f32_32x32x16_f16 v[80:95], v[96:99], v[142:145], v[80:95]
	v_or_b32_e32 v107, 0x400, v106
	global_load_dword v224, v108, s[8:9] offset:2048
	global_load_dword v225, v108, s[10:11] offset:2048
	global_load_dword v222, v108, s[8:9] offset:2304
	global_load_dword v223, v108, s[10:11] offset:2304
	global_load_dword v220, v108, s[8:9] offset:3072
	global_load_dword v221, v108, s[10:11] offset:3072
	global_load_dword v218, v108, s[8:9] offset:3328
	global_load_dword v219, v108, s[10:11] offset:3328
	v_or_b32_e32 v108, v107, v113
	v_or_b32_e32 v107, v107, v112
	v_lshlrev_b32_e32 v108, 2, v108
	v_lshlrev_b32_e32 v107, 2, v107
	global_load_dword v184, v108, s[8:9]
	global_load_dword v185, v108, s[10:11]
	v_mfma_f32_32x32x16_f16 v[48:63], v[96:99], v[150:153], v[48:63]
	global_load_dword v216, v107, s[8:9]
	global_load_dword v217, v107, s[10:11]
	v_mfma_f32_32x32x16_f16 v[16:31], v[96:99], v[158:161], v[16:31]
	v_or_b32_e32 v96, 0x440, v106
	v_or_b32_e32 v97, v96, v113
	v_or_b32_e32 v96, v96, v112
	v_lshlrev_b32_e32 v97, 2, v97
	v_lshlrev_b32_e32 v96, 2, v96
	global_load_dword v182, v97, s[8:9]
	global_load_dword v183, v97, s[10:11]
	global_load_dword v214, v96, s[8:9]
	global_load_dword v215, v96, s[10:11]
	v_or_b32_e32 v96, 0x500, v106
	v_or_b32_e32 v97, v96, v113
	v_or_b32_e32 v96, v96, v112
	v_lshlrev_b32_e32 v97, 2, v97
	v_lshlrev_b32_e32 v96, 2, v96
	global_load_dword v180, v97, s[8:9]
	global_load_dword v181, v97, s[10:11]
	global_load_dword v212, v96, s[8:9]
	global_load_dword v213, v96, s[10:11]
	v_or_b32_e32 v96, 0x540, v106
	v_or_b32_e32 v97, v96, v113
	v_or_b32_e32 v96, v96, v112
	v_lshlrev_b32_e32 v97, 2, v97
	v_lshlrev_b32_e32 v96, 2, v96
	global_load_dword v178, v97, s[8:9]
	global_load_dword v179, v97, s[10:11]
	global_load_dword v210, v96, s[8:9]
	global_load_dword v211, v96, s[10:11]
	v_or_b32_e32 v96, 0x600, v106
	v_or_b32_e32 v97, v96, v113
	v_or_b32_e32 v96, v96, v112
	v_lshlrev_b32_e32 v97, 2, v97
	v_lshlrev_b32_e32 v96, 2, v96
	global_load_dword v176, v97, s[8:9]
	global_load_dword v177, v97, s[10:11]
	global_load_dword v208, v96, s[8:9]
	global_load_dword v209, v96, s[10:11]
	v_or_b32_e32 v96, 0x640, v106
	v_or_b32_e32 v97, v96, v113
	v_or_b32_e32 v96, v96, v112
	v_lshlrev_b32_e32 v97, 2, v97
	v_lshlrev_b32_e32 v96, 2, v96
	global_load_dword v174, v97, s[8:9]
	global_load_dword v175, v97, s[10:11]
	global_load_dword v206, v96, s[8:9]
	global_load_dword v207, v96, s[10:11]
	v_or_b32_e32 v96, 0x700, v106
	v_or_b32_e32 v97, v96, v113
	v_or_b32_e32 v96, v96, v112
	v_lshlrev_b32_e32 v97, 2, v97
	v_lshlrev_b32_e32 v96, 2, v96
	global_load_dword v172, v97, s[8:9]
	global_load_dword v173, v97, s[10:11]
	global_load_dword v204, v96, s[8:9]
	global_load_dword v205, v96, s[10:11]
	v_or_b32_e32 v96, 0x740, v106
	v_or_b32_e32 v97, v96, v113
	v_or_b32_e32 v96, v96, v112
	v_lshlrev_b32_e32 v97, 2, v97
	v_lshlrev_b32_e32 v96, 2, v96
	global_load_dword v170, v97, s[8:9]
	global_load_dword v171, v97, s[10:11]
	global_load_dword v202, v96, s[8:9]
	global_load_dword v203, v96, s[10:11]
	v_mfma_f32_32x32x16_f16 v[64:79], v[138:141], v[118:121], v[64:79]
	v_mfma_f32_32x32x16_f16 v[32:47], v[138:141], v[126:129], v[32:47]
	v_mfma_f32_32x32x16_f16 v[0:15], v[138:141], v[134:137], v[0:15]
	v_mfma_f32_32x32x16_f16 v[64:79], v[122:125], v[142:145], v[64:79]
	v_mfma_f32_32x32x16_f16 v[32:47], v[122:125], v[150:153], v[32:47]
	v_mfma_f32_32x32x16_f16 v[0:15], v[122:125], v[158:161], v[0:15]
	v_mfma_f32_32x32x16_f16 v[80:95], v[100:103], v[146:149], v[80:95]
	v_mfma_f32_32x32x16_f16 v[48:63], v[100:103], v[154:157], v[48:63]
	v_mfma_f32_32x32x16_f16 v[16:31], v[100:103], v[114:117], v[16:31]
	v_mfma_f32_32x32x16_f16 v[64:79], v[130:133], v[146:149], v[64:79]
	v_mfma_f32_32x32x16_f16 v[32:47], v[130:133], v[154:157], v[32:47]
	v_mfma_f32_32x32x16_f16 v[0:15], v[130:133], v[114:117], v[0:15]
	ds_read_b128 v[128:131], v104 offset:64512
	ds_read_b128 v[106:109], v105
	ds_read_b128 v[100:103], v169 offset:64512
	ds_read_b128 v[132:135], v104 offset:64544
	ds_read_b128 v[160:163], v105 offset:32
	v_mbcnt_lo_u32_b32 v110, -1, 0
	s_waitcnt lgkmcnt(3)
	v_mfma_f32_32x32x16_f16 v[80:95], v[128:131], v[106:109], v[80:95]
	v_mbcnt_hi_u32_b32 v110, -1, v110
	v_and_b32_e32 v111, 64, v110
	ds_read_b128 v[96:99], v169 offset:64544
	ds_read_b128 v[148:151], v105 offset:4608
	ds_read_b128 v[144:147], v105 offset:4640
	v_add_u32_e32 v111, 64, v111
	ds_read_b128 v[140:143], v104 offset:64576
	ds_read_b128 v[136:139], v104 offset:64608
	ds_read_b128 v[124:127], v105 offset:9216
	ds_read_b128 v[120:123], v105 offset:9248
	s_lshr_b32 s0, s0, 7
	s_and_b32 s8, s0, 0xfffff0
	s_waitcnt lgkmcnt(7)
	v_mfma_f32_32x32x16_f16 v[80:95], v[132:135], v[160:163], v[80:95]
	s_bfe_u32 s2, s14, 0x40006
	s_cmpk_lt_u32 s14, 0x400
	s_cselect_b64 s[0:1], -1, 0
	s_and_b32 s9, s14, 0x7ffffc00
	v_mov_b32_e32 v228, 0x3e38aa3b
	s_cmpk_eq_i32 s9, 0x400
	s_cselect_b32 s9, s6, s12
	v_mfma_f32_32x32x16_f16 v[64:79], v[100:103], v[106:109], v[64:79]
	v_xor_b32_e32 v106, 1, v110
	v_cmp_lt_i32_e32 vcc, v106, v111
	s_cselect_b32 s10, s7, s13
	s_nop 0
	v_cndmask_b32_e32 v235, v110, v106, vcc
	ds_read_b128 v[236:239], v105 offset:64
	ds_read_b128 v[240:243], v105 offset:96
	ds_read_b128 v[156:159], v105 offset:4672
	ds_read_b128 v[152:155], v105 offset:4704
	ds_read_b128 v[112:115], v105 offset:9280
	ds_read_b128 v[104:107], v105 offset:9312
	ds_read_b128 v[116:119], v169 offset:64576
	ds_read_b128 v[108:111], v169 offset:64608
	v_cmp_eq_u32_e32 vcc, 0, v164
	s_waitcnt lgkmcnt(7)
	v_mfma_f32_32x32x16_f16 v[80:95], v[140:143], v[236:239], v[80:95]
	s_waitcnt lgkmcnt(0)
	s_barrier
	v_lshlrev_b32_e32 v169, 2, v235
	v_cndmask_b32_e64 v235, 1.0, v228, s[0:1]
	s_and_b64 s[0:1], s[0:1], exec
	s_cselect_b32 s16, s5, s10
	v_mfma_f32_32x32x16_f16 v[80:95], v[136:139], v[240:243], v[80:95]
	s_cselect_b32 s9, s4, s9
	s_cmpk_lt_u32 s14, 0x800
	s_cselect_b64 s[0:1], -1, 0
	s_waitcnt vmcnt(62)
	v_cndmask_b32_e64 v244, 0, v201, s[0:1]
	s_nop 6
	v_cndmask_b32_e32 v164, v80, v81, vcc
	ds_bpermute_b32 v164, v169, v164
	s_or_b32 s2, s2, s8
	s_lshl_b64 s[10:11], s[2:3], 18
	s_add_u32 s10, s9, s10
	s_addc_u32 s11, s16, s11
	s_waitcnt lgkmcnt(0)
	v_cndmask_b32_e32 v81, v81, v164, vcc
	v_cndmask_b32_e32 v80, v164, v80, vcc
	v_cndmask_b32_e64 v164, 1.0, v200, s[0:1]
	v_mul_f32_e32 v245, v81, v244
	v_fma_f32 v245, v80, v164, -v245
	v_mul_f32_e32 v80, v80, v244
	v_fmac_f32_e32 v80, v81, v164
	v_bitop3_b32 v81, s15, 62, v166 bitop3:0xc8
	v_lshlrev_b32_e32 v164, 1, v81
	v_mul_f32_e32 v81, v235, v245
	v_mul_f32_e32 v80, v235, v80
	v_cvt_pk_f16_f32 v246, v81, v80
	v_lshlrev_b32_e32 v80, 7, v167
	v_and_b32_e32 v80, 0x3e280, v80
	v_mov_b32_e32 v81, v165
	v_lshl_add_u64 v[166:167], s[10:11], 0, v[164:165]
	v_lshl_add_u64 v[244:245], v[166:167], 0, v[80:81]
	global_store_dword v[244:245], v246, off
	s_waitcnt vmcnt(61)
	v_cndmask_b32_e64 v247, 0, v199, s[0:1]
	v_cndmask_b32_e32 v246, v82, v83, vcc
	ds_bpermute_b32 v246, v169, v246
	v_mfma_f32_32x32x16_f16 v[64:79], v[96:99], v[160:163], v[64:79]
	s_add_i32 s2, s14, 32
	s_bfe_u32 s9, s2, 0x40006
	s_cmpk_lt_u32 s14, 0x3e0
	s_waitcnt lgkmcnt(0)
	v_cndmask_b32_e32 v83, v83, v246, vcc
	v_cndmask_b32_e32 v82, v246, v82, vcc
	v_cndmask_b32_e64 v246, 1.0, v198, s[0:1]
	v_mul_f32_e32 v248, v83, v247
	v_fma_f32 v248, v82, v246, -v248
	v_mul_f32_e32 v82, v82, v247
	v_fmac_f32_e32 v82, v83, v246
	v_mul_f32_e32 v83, v235, v248
	v_mul_f32_e32 v82, v235, v82
	v_cvt_pk_f16_f32 v82, v83, v82
	global_store_dword v[244:245], v82, off offset:256
	v_mov_b32_e32 v82, v85
	s_waitcnt vmcnt(60)
	v_cndmask_b32_e64 v85, 0, v197, s[0:1]
	v_cndmask_b32_e32 v83, v84, v82, vcc
	ds_bpermute_b32 v83, v169, v83
	v_mfma_f32_32x32x16_f16 v[64:79], v[116:119], v[236:239], v[64:79]
	s_waitcnt lgkmcnt(0)
	v_cndmask_b32_e32 v82, v82, v83, vcc
	v_cndmask_b32_e32 v83, v83, v84, vcc
	v_cndmask_b32_e64 v84, 1.0, v196, s[0:1]
	v_mul_f32_e32 v246, v82, v85
	v_fma_f32 v246, v83, v84, -v246
	v_mul_f32_e32 v83, v83, v85
	v_fmac_f32_e32 v83, v82, v84
	v_mul_f32_e32 v82, v235, v246
	v_mul_f32_e32 v83, v235, v83
	v_cvt_pk_f16_f32 v82, v82, v83
	global_store_dword v[244:245], v82, off offset:1024
	v_mov_b32_e32 v82, v87
	s_waitcnt vmcnt(59)
	v_cndmask_b32_e64 v85, 0, v195, s[0:1]
	v_cndmask_b32_e32 v83, v86, v82, vcc
	ds_bpermute_b32 v83, v169, v83
	v_cndmask_b32_e64 v84, 1.0, v194, s[0:1]
	v_mfma_f32_32x32x16_f16 v[64:79], v[108:111], v[240:243], v[64:79]
	s_waitcnt lgkmcnt(0)
	v_cndmask_b32_e32 v82, v82, v83, vcc
	v_cndmask_b32_e32 v83, v83, v86, vcc
	v_mul_f32_e32 v86, v82, v85
	v_fma_f32 v86, v83, v84, -v86
	v_mul_f32_e32 v83, v83, v85
	v_fmac_f32_e32 v83, v82, v84
	v_mul_f32_e32 v82, v235, v86
	v_mul_f32_e32 v83, v235, v83
	v_cvt_pk_f16_f32 v82, v82, v83
	global_store_dword v[244:245], v82, off offset:1280
	v_mov_b32_e32 v82, v89
	s_waitcnt vmcnt(50)
	v_cndmask_b32_e64 v85, 0, v193, s[0:1]
	v_cndmask_b32_e32 v83, v88, v82, vcc
	ds_bpermute_b32 v83, v169, v83
	v_cndmask_b32_e64 v84, 1.0, v192, s[0:1]
	v_mfma_f32_32x32x16_f16 v[48:63], v[128:131], v[148:151], v[48:63]
	s_waitcnt lgkmcnt(0)
	v_cndmask_b32_e32 v82, v82, v83, vcc
	v_cndmask_b32_e32 v83, v83, v88, vcc
	v_mul_f32_e32 v86, v82, v85
	v_fma_f32 v86, v83, v84, -v86
	v_mul_f32_e32 v83, v83, v85
	v_fmac_f32_e32 v83, v82, v84
	v_mul_f32_e32 v82, v235, v86
	v_mul_f32_e32 v83, v235, v83
	v_cvt_pk_f16_f32 v82, v82, v83
	global_store_dword v[244:245], v82, off offset:2048
	v_mov_b32_e32 v82, v91
	s_waitcnt vmcnt(49)
	v_cndmask_b32_e64 v85, 0, v191, s[0:1]
	v_cndmask_b32_e32 v83, v90, v82, vcc
	ds_bpermute_b32 v83, v169, v83
	v_cndmask_b32_e64 v84, 1.0, v190, s[0:1]
	v_mfma_f32_32x32x16_f16 v[48:63], v[132:135], v[144:147], v[48:63]
	s_waitcnt lgkmcnt(0)
	v_cndmask_b32_e32 v82, v82, v83, vcc
	v_cndmask_b32_e32 v83, v83, v90, vcc
	v_mul_f32_e32 v86, v82, v85
	v_fma_f32 v86, v83, v84, -v86
	v_mul_f32_e32 v83, v83, v85
	v_fmac_f32_e32 v83, v82, v84
	v_mul_f32_e32 v82, v235, v86
	v_mul_f32_e32 v83, v235, v83
	v_cvt_pk_f16_f32 v82, v82, v83
	global_store_dword v[244:245], v82, off offset:2304
	v_mov_b32_e32 v82, v93
	s_waitcnt vmcnt(48)
	v_cndmask_b32_e64 v85, 0, v189, s[0:1]
	v_cndmask_b32_e32 v83, v92, v82, vcc
	ds_bpermute_b32 v83, v169, v83
	v_cndmask_b32_e64 v84, 1.0, v188, s[0:1]
	v_mfma_f32_32x32x16_f16 v[48:63], v[140:143], v[156:159], v[48:63]
	s_waitcnt lgkmcnt(0)
	v_cndmask_b32_e32 v82, v82, v83, vcc
	v_cndmask_b32_e32 v83, v83, v92, vcc
	v_mul_f32_e32 v86, v82, v85
	v_fma_f32 v86, v83, v84, -v86
	v_mul_f32_e32 v83, v83, v85
	v_fmac_f32_e32 v83, v82, v84
	v_mul_f32_e32 v82, v235, v86
	v_mul_f32_e32 v83, v235, v83
	v_cvt_pk_f16_f32 v82, v82, v83
	global_store_dword v[244:245], v82, off offset:3072
	v_mov_b32_e32 v82, v95
	s_waitcnt vmcnt(47)
	v_cndmask_b32_e64 v85, 0, v187, s[0:1]
	v_cndmask_b32_e32 v83, v94, v82, vcc
	ds_bpermute_b32 v83, v169, v83
	v_mfma_f32_32x32x16_f16 v[48:63], v[136:139], v[152:155], v[48:63]
	s_waitcnt lgkmcnt(0)
	v_cndmask_b32_e32 v82, v82, v83, vcc
	v_cndmask_b32_e32 v84, v83, v94, vcc
	v_cndmask_b32_e64 v83, 1.0, v186, s[0:1]
	v_mul_f32_e32 v86, v82, v85
	v_fma_f32 v86, v84, v83, -v86
	v_mul_f32_e32 v84, v84, v85
	v_fmac_f32_e32 v84, v82, v83
	v_mul_f32_e32 v82, v235, v86
	v_mul_f32_e32 v83, v235, v84
	v_cvt_pk_f16_f32 v82, v82, v83
	global_store_dword v[244:245], v82, off offset:3328
	s_waitcnt vmcnt(38)
	v_cndmask_b32_e64 v83, 0, v185, s[0:1]
	v_cndmask_b32_e32 v82, v64, v65, vcc
	ds_bpermute_b32 v82, v169, v82
	v_mfma_f32_32x32x16_f16 v[32:47], v[100:103], v[148:151], v[32:47]
	s_waitcnt lgkmcnt(0)
	v_cndmask_b32_e32 v65, v65, v82, vcc
	v_cndmask_b32_e32 v64, v82, v64, vcc
	v_cndmask_b32_e64 v82, 1.0, v184, s[0:1]
	v_mul_f32_e32 v84, v65, v83
	v_fma_f32 v84, v64, v82, -v84
	v_mul_f32_e32 v64, v64, v83
	v_fmac_f32_e32 v64, v65, v82
	v_mul_f32_e32 v65, v235, v84
	v_mul_f32_e32 v64, v235, v64
	v_cvt_pk_f16_f32 v84, v65, v64
	v_or_b32_e32 v64, 0x1000, v80
	v_mov_b32_e32 v65, v165
	v_lshl_add_u64 v[82:83], v[166:167], 0, v[64:65]
	global_store_dword v[82:83], v84, off
	s_waitcnt vmcnt(35)
	v_cndmask_b32_e64 v83, 0, v183, s[0:1]
	v_cndmask_b32_e32 v82, v66, v67, vcc
	ds_bpermute_b32 v82, v169, v82
	v_mfma_f32_32x32x16_f16 v[32:47], v[96:99], v[144:147], v[32:47]
	s_waitcnt lgkmcnt(0)
	v_cndmask_b32_e32 v67, v67, v82, vcc
	v_cndmask_b32_e32 v66, v82, v66, vcc
	v_cndmask_b32_e64 v82, 1.0, v182, s[0:1]
	v_mul_f32_e32 v84, v67, v83
	v_fma_f32 v84, v66, v82, -v84
	v_mul_f32_e32 v66, v66, v83
	v_fmac_f32_e32 v66, v67, v82
	v_mul_f32_e32 v67, v235, v84
	v_mul_f32_e32 v66, v235, v66
	v_cvt_pk_f16_f32 v84, v67, v66
	v_or_b32_e32 v66, 0x1100, v80
	v_mov_b32_e32 v67, v165
	v_lshl_add_u64 v[82:83], v[166:167], 0, v[66:67]
	global_store_dword v[82:83], v84, off
	s_waitcnt vmcnt(32)
	v_cndmask_b32_e64 v83, 0, v181, s[0:1]
	v_cndmask_b32_e32 v82, v68, v69, vcc
	ds_bpermute_b32 v82, v169, v82
	v_mfma_f32_32x32x16_f16 v[32:47], v[116:119], v[156:159], v[32:47]
	s_waitcnt lgkmcnt(0)
	v_cndmask_b32_e32 v69, v69, v82, vcc
	v_cndmask_b32_e32 v68, v82, v68, vcc
	v_cndmask_b32_e64 v82, 1.0, v180, s[0:1]
	v_mul_f32_e32 v84, v69, v83
	v_fma_f32 v84, v68, v82, -v84
	v_mul_f32_e32 v68, v68, v83
	v_fmac_f32_e32 v68, v69, v82
	v_mul_f32_e32 v69, v235, v84
	v_mul_f32_e32 v68, v235, v68
	v_cvt_pk_f16_f32 v84, v69, v68
	v_or_b32_e32 v68, 0x1400, v80
	v_mov_b32_e32 v69, v165
	v_lshl_add_u64 v[82:83], v[166:167], 0, v[68:69]
	global_store_dword v[82:83], v84, off
	s_waitcnt vmcnt(29)
	v_cndmask_b32_e64 v83, 0, v179, s[0:1]
	v_cndmask_b32_e32 v82, v70, v71, vcc
	ds_bpermute_b32 v82, v169, v82
	v_mfma_f32_32x32x16_f16 v[32:47], v[108:111], v[152:155], v[32:47]
	s_waitcnt lgkmcnt(0)
	v_cndmask_b32_e32 v71, v71, v82, vcc
	v_cndmask_b32_e32 v70, v82, v70, vcc
	v_cndmask_b32_e64 v82, 1.0, v178, s[0:1]
	v_mul_f32_e32 v84, v71, v83
	v_fma_f32 v84, v70, v82, -v84
	v_mul_f32_e32 v70, v70, v83
	v_fmac_f32_e32 v70, v71, v82
	v_mul_f32_e32 v71, v235, v84
	v_mul_f32_e32 v70, v235, v70
	v_cvt_pk_f16_f32 v84, v71, v70
	v_or_b32_e32 v70, 0x1500, v80
	v_mov_b32_e32 v71, v165
	v_lshl_add_u64 v[82:83], v[166:167], 0, v[70:71]
	global_store_dword v[82:83], v84, off
	s_waitcnt vmcnt(26)
	v_cndmask_b32_e64 v83, 0, v177, s[0:1]
	v_cndmask_b32_e32 v82, v72, v73, vcc
	ds_bpermute_b32 v82, v169, v82
	v_mfma_f32_32x32x16_f16 v[16:31], v[128:131], v[124:127], v[16:31]
	s_waitcnt lgkmcnt(0)
	v_cndmask_b32_e32 v73, v73, v82, vcc
	v_cndmask_b32_e32 v72, v82, v72, vcc
	v_cndmask_b32_e64 v82, 1.0, v176, s[0:1]
	v_mul_f32_e32 v84, v73, v83
	v_fma_f32 v84, v72, v82, -v84
	v_mul_f32_e32 v72, v72, v83
	v_fmac_f32_e32 v72, v73, v82
	v_mul_f32_e32 v73, v235, v84
	v_mul_f32_e32 v72, v235, v72
	v_cvt_pk_f16_f32 v84, v73, v72
	v_or_b32_e32 v72, 0x1800, v80
	v_mov_b32_e32 v73, v165
	v_lshl_add_u64 v[82:83], v[166:167], 0, v[72:73]
	global_store_dword v[82:83], v84, off
	s_waitcnt vmcnt(23)
	v_cndmask_b32_e64 v83, 0, v175, s[0:1]
	v_cndmask_b32_e32 v82, v74, v75, vcc
	ds_bpermute_b32 v82, v169, v82
	v_mfma_f32_32x32x16_f16 v[16:31], v[132:135], v[120:123], v[16:31]
	s_waitcnt lgkmcnt(0)
	v_cndmask_b32_e32 v75, v75, v82, vcc
	v_cndmask_b32_e32 v74, v82, v74, vcc
	v_cndmask_b32_e64 v82, 1.0, v174, s[0:1]
	v_mul_f32_e32 v84, v75, v83
	v_fma_f32 v84, v74, v82, -v84
	v_mul_f32_e32 v74, v74, v83
	v_fmac_f32_e32 v74, v75, v82
	v_mul_f32_e32 v75, v235, v84
	v_mul_f32_e32 v74, v235, v74
	v_cvt_pk_f16_f32 v84, v75, v74
	v_or_b32_e32 v74, 0x1900, v80
	v_mov_b32_e32 v75, v165
	v_lshl_add_u64 v[82:83], v[166:167], 0, v[74:75]
	global_store_dword v[82:83], v84, off
	s_waitcnt vmcnt(20)
	v_cndmask_b32_e64 v83, 0, v173, s[0:1]
	v_cndmask_b32_e32 v82, v76, v77, vcc
	ds_bpermute_b32 v82, v169, v82
	v_mfma_f32_32x32x16_f16 v[16:31], v[140:143], v[112:115], v[16:31]
	s_waitcnt lgkmcnt(0)
	v_cndmask_b32_e32 v77, v77, v82, vcc
	v_cndmask_b32_e32 v76, v82, v76, vcc
	v_cndmask_b32_e64 v82, 1.0, v172, s[0:1]
	v_mul_f32_e32 v84, v77, v83
	v_fma_f32 v84, v76, v82, -v84
	v_mul_f32_e32 v76, v76, v83
	v_fmac_f32_e32 v76, v77, v82
	v_mul_f32_e32 v77, v235, v84
	v_mul_f32_e32 v76, v235, v76
	v_cvt_pk_f16_f32 v84, v77, v76
	v_or_b32_e32 v76, 0x1c00, v80
	v_mov_b32_e32 v77, v165
	v_lshl_add_u64 v[82:83], v[166:167], 0, v[76:77]
	global_store_dword v[82:83], v84, off
	s_waitcnt vmcnt(17)
	v_cndmask_b32_e64 v83, 0, v171, s[0:1]
	v_cndmask_b32_e32 v82, v78, v79, vcc
	ds_bpermute_b32 v82, v169, v82
	v_mfma_f32_32x32x16_f16 v[16:31], v[136:139], v[104:107], v[16:31]
	s_waitcnt lgkmcnt(0)
	v_cndmask_b32_e32 v79, v79, v82, vcc
	v_cndmask_b32_e32 v78, v82, v78, vcc
	v_cndmask_b32_e64 v82, 1.0, v170, s[0:1]
	v_mul_f32_e32 v84, v79, v83
	v_fma_f32 v84, v78, v82, -v84
	v_mul_f32_e32 v78, v78, v83
	v_fmac_f32_e32 v78, v79, v82
	v_mul_f32_e32 v79, v235, v84
	v_mul_f32_e32 v78, v235, v78
	v_cvt_pk_f16_f32 v84, v79, v78
	v_or_b32_e32 v78, 0x1d00, v80
	v_mov_b32_e32 v79, v165
	v_lshl_add_u64 v[82:83], v[166:167], 0, v[78:79]
	global_store_dword v[82:83], v84, off
	s_cselect_b64 s[0:1], -1, 0
	v_cndmask_b32_e32 v82, v48, v49, vcc
	s_and_b32 s2, s2, 0x7ffffc00
	ds_bpermute_b32 v82, v169, v82
	s_cmpk_eq_i32 s2, 0x400
	s_cselect_b32 s2, s6, s12
	s_cselect_b32 s10, s7, s13
	v_cndmask_b32_e64 v84, 1.0, v228, s[0:1]
	s_and_b64 s[0:1], s[0:1], exec
	s_cselect_b32 s15, s5, s10
	s_cselect_b32 s16, s4, s2
	s_cmpk_lt_u32 s14, 0x7e0
	s_cselect_b64 s[0:1], -1, 0
	s_waitcnt lgkmcnt(0)
	v_cndmask_b32_e32 v49, v49, v82, vcc
	v_cndmask_b32_e64 v83, 0, v234, s[0:1]
	v_cndmask_b32_e32 v48, v82, v48, vcc
	v_cndmask_b32_e64 v82, 1.0, v233, s[0:1]
	v_mul_f32_e32 v85, v49, v83
	v_fma_f32 v85, v48, v82, -v85
	v_mul_f32_e32 v48, v48, v83
	v_fmac_f32_e32 v48, v49, v82
	s_or_b32 s2, s9, s8
	v_mul_f32_e32 v49, v84, v85
	v_mul_f32_e32 v48, v84, v48
	s_lshl_b64 s[10:11], s[2:3], 18
	v_cvt_pk_f16_f32 v85, v49, v48
	v_bitop3_b32 v48, v168, 62, 32 bitop3:0x48
	s_add_u32 s10, s16, s10
	s_addc_u32 s11, s15, s11
	v_lshlrev_b32_e32 v48, 1, v48
	v_mov_b32_e32 v49, v165
	v_lshl_add_u64 v[48:49], s[10:11], 0, v[48:49]
	v_lshl_add_u64 v[82:83], v[48:49], 0, v[80:81]
	global_store_dword v[82:83], v85, off
	v_cndmask_b32_e64 v86, 0, v232, s[0:1]
	v_cndmask_b32_e32 v85, v50, v51, vcc
	ds_bpermute_b32 v85, v169, v85
	s_add_i32 s2, s14, 64
	s_bfe_u32 s9, s2, 0x40006
	s_cmpk_lt_u32 s14, 0x3c0
	v_mfma_f32_32x32x16_f16 v[0:15], v[100:103], v[124:127], v[0:15]
	s_waitcnt lgkmcnt(0)
	v_cndmask_b32_e32 v51, v51, v85, vcc
	v_cndmask_b32_e32 v50, v85, v50, vcc
	v_cndmask_b32_e64 v85, 1.0, v231, s[0:1]
	v_mul_f32_e32 v87, v51, v86
	v_fma_f32 v87, v50, v85, -v87
	v_mul_f32_e32 v50, v50, v86
	v_fmac_f32_e32 v50, v51, v85
	v_mul_f32_e32 v51, v84, v87
	v_mul_f32_e32 v50, v84, v50
	v_cvt_pk_f16_f32 v50, v51, v50
	global_store_dword v[82:83], v50, off offset:256
	v_mov_b32_e32 v50, v53
	v_cndmask_b32_e64 v53, 0, v230, s[0:1]
	v_cndmask_b32_e32 v51, v52, v50, vcc
	ds_bpermute_b32 v51, v169, v51
	v_mfma_f32_32x32x16_f16 v[0:15], v[96:99], v[120:123], v[0:15]
	s_waitcnt lgkmcnt(0)
	v_cndmask_b32_e32 v50, v50, v51, vcc
	v_cndmask_b32_e32 v51, v51, v52, vcc
	v_cndmask_b32_e64 v52, 1.0, v229, s[0:1]
	v_mul_f32_e32 v85, v50, v53
	v_fma_f32 v85, v51, v52, -v85
	v_mul_f32_e32 v51, v51, v53
	v_fmac_f32_e32 v51, v50, v52
	v_mul_f32_e32 v50, v84, v85
	v_mul_f32_e32 v51, v84, v51
	v_cvt_pk_f16_f32 v50, v50, v51
	global_store_dword v[82:83], v50, off offset:1024
	v_mov_b32_e32 v50, v55
	v_cndmask_b32_e64 v53, 0, v227, s[0:1]
	v_cndmask_b32_e32 v51, v54, v50, vcc
	ds_bpermute_b32 v51, v169, v51
	v_cndmask_b32_e64 v52, 1.0, v226, s[0:1]
	v_mfma_f32_32x32x16_f16 v[0:15], v[116:119], v[112:115], v[0:15]
	s_waitcnt lgkmcnt(0)
	v_cndmask_b32_e32 v50, v50, v51, vcc
	v_cndmask_b32_e32 v51, v51, v54, vcc
	v_mul_f32_e32 v54, v50, v53
	v_fma_f32 v54, v51, v52, -v54
	v_mul_f32_e32 v51, v51, v53
	v_fmac_f32_e32 v51, v50, v52
	v_mul_f32_e32 v50, v84, v54
	v_mul_f32_e32 v51, v84, v51
	v_cvt_pk_f16_f32 v50, v50, v51
	global_store_dword v[82:83], v50, off offset:1280
	v_mov_b32_e32 v50, v57
	v_cndmask_b32_e64 v53, 0, v225, s[0:1]
	v_cndmask_b32_e32 v51, v56, v50, vcc
	ds_bpermute_b32 v51, v169, v51
	v_cndmask_b32_e64 v52, 1.0, v224, s[0:1]
	v_mfma_f32_32x32x16_f16 v[0:15], v[108:111], v[104:107], v[0:15]
	s_waitcnt lgkmcnt(0)
	v_cndmask_b32_e32 v50, v50, v51, vcc
	v_cndmask_b32_e32 v51, v51, v56, vcc
	v_mul_f32_e32 v54, v50, v53
	v_fma_f32 v54, v51, v52, -v54
	v_mul_f32_e32 v51, v51, v53
	v_fmac_f32_e32 v51, v50, v52
	v_mul_f32_e32 v50, v84, v54
	v_mul_f32_e32 v51, v84, v51
	v_cvt_pk_f16_f32 v50, v50, v51
	global_store_dword v[82:83], v50, off offset:2048
	v_mov_b32_e32 v50, v59
	v_cndmask_b32_e64 v53, 0, v223, s[0:1]
	v_cndmask_b32_e32 v51, v58, v50, vcc
	ds_bpermute_b32 v51, v169, v51
	v_cndmask_b32_e64 v52, 1.0, v222, s[0:1]
	s_waitcnt lgkmcnt(0)
	v_cndmask_b32_e32 v50, v50, v51, vcc
	v_cndmask_b32_e32 v51, v51, v58, vcc
	v_mul_f32_e32 v54, v50, v53
	v_fma_f32 v54, v51, v52, -v54
	v_mul_f32_e32 v51, v51, v53
	v_fmac_f32_e32 v51, v50, v52
	v_mul_f32_e32 v50, v84, v54
	v_mul_f32_e32 v51, v84, v51
	v_cvt_pk_f16_f32 v50, v50, v51
	global_store_dword v[82:83], v50, off offset:2304
	v_mov_b32_e32 v50, v61
	v_cndmask_b32_e64 v53, 0, v221, s[0:1]
	v_cndmask_b32_e32 v51, v60, v50, vcc
	ds_bpermute_b32 v51, v169, v51
	v_cndmask_b32_e64 v52, 1.0, v220, s[0:1]
	s_waitcnt lgkmcnt(0)
	v_cndmask_b32_e32 v50, v50, v51, vcc
	v_cndmask_b32_e32 v51, v51, v60, vcc
	v_mul_f32_e32 v54, v50, v53
	v_fma_f32 v54, v51, v52, -v54
	v_mul_f32_e32 v51, v51, v53
	v_fmac_f32_e32 v51, v50, v52
	v_mul_f32_e32 v50, v84, v54
	v_mul_f32_e32 v51, v84, v51
	v_cvt_pk_f16_f32 v50, v50, v51
	global_store_dword v[82:83], v50, off offset:3072
	v_mov_b32_e32 v50, v63
	v_cndmask_b32_e64 v53, 0, v219, s[0:1]
	v_cndmask_b32_e32 v51, v62, v50, vcc
	ds_bpermute_b32 v51, v169, v51
	s_waitcnt lgkmcnt(0)
	v_cndmask_b32_e32 v50, v50, v51, vcc
	v_cndmask_b32_e32 v52, v51, v62, vcc
	v_cndmask_b32_e64 v51, 1.0, v218, s[0:1]
	v_mul_f32_e32 v54, v50, v53
	v_fma_f32 v54, v52, v51, -v54
	v_mul_f32_e32 v52, v52, v53
	v_fmac_f32_e32 v52, v50, v51
	v_mul_f32_e32 v50, v84, v54
	v_mul_f32_e32 v51, v84, v52
	v_cvt_pk_f16_f32 v50, v50, v51
	global_store_dword v[82:83], v50, off offset:3328
	v_cndmask_b32_e64 v51, 0, v217, s[0:1]
	v_cndmask_b32_e32 v50, v32, v33, vcc
	ds_bpermute_b32 v50, v169, v50
	s_waitcnt lgkmcnt(0)
	v_cndmask_b32_e32 v33, v33, v50, vcc
	v_cndmask_b32_e32 v32, v50, v32, vcc
	v_cndmask_b32_e64 v50, 1.0, v216, s[0:1]
	v_mul_f32_e32 v52, v33, v51
	v_fma_f32 v52, v32, v50, -v52
	v_mul_f32_e32 v32, v32, v51
	v_fmac_f32_e32 v32, v33, v50
	v_mul_f32_e32 v33, v84, v52
	v_mul_f32_e32 v32, v84, v32
	v_cvt_pk_f16_f32 v50, v33, v32
	v_lshl_add_u64 v[32:33], v[48:49], 0, v[64:65]
	global_store_dword v[32:33], v50, off
	v_mov_b32_e32 v32, v35
	v_cndmask_b32_e64 v35, 0, v215, s[0:1]
	v_cndmask_b32_e32 v33, v34, v32, vcc
	ds_bpermute_b32 v33, v169, v33
	s_waitcnt lgkmcnt(0)
	v_cndmask_b32_e32 v32, v32, v33, vcc
	v_cndmask_b32_e32 v33, v33, v34, vcc
	v_cndmask_b32_e64 v34, 1.0, v214, s[0:1]
	v_mul_f32_e32 v50, v32, v35
	v_fma_f32 v50, v33, v34, -v50
	v_mul_f32_e32 v33, v33, v35
	v_fmac_f32_e32 v33, v32, v34
	v_mul_f32_e32 v32, v84, v50
	v_mul_f32_e32 v33, v84, v33
	v_cvt_pk_f16_f32 v34, v32, v33
	v_lshl_add_u64 v[32:33], v[48:49], 0, v[66:67]
	global_store_dword v[32:33], v34, off
	v_mov_b32_e32 v32, v37
	v_cndmask_b32_e64 v35, 0, v213, s[0:1]
	v_cndmask_b32_e32 v33, v36, v32, vcc
	ds_bpermute_b32 v33, v169, v33
	v_cndmask_b32_e64 v34, 1.0, v212, s[0:1]
	s_waitcnt lgkmcnt(0)
	v_cndmask_b32_e32 v32, v32, v33, vcc
	v_cndmask_b32_e32 v33, v33, v36, vcc
	v_mul_f32_e32 v36, v32, v35
	v_fma_f32 v36, v33, v34, -v36
	v_mul_f32_e32 v33, v33, v35
	v_fmac_f32_e32 v33, v32, v34
	v_mul_f32_e32 v32, v84, v36
	v_mul_f32_e32 v33, v84, v33
	v_cvt_pk_f16_f32 v34, v32, v33
	v_lshl_add_u64 v[32:33], v[48:49], 0, v[68:69]
	global_store_dword v[32:33], v34, off
	v_mov_b32_e32 v32, v39
	v_cndmask_b32_e64 v35, 0, v211, s[0:1]
	v_cndmask_b32_e32 v33, v38, v32, vcc
	ds_bpermute_b32 v33, v169, v33
	v_cndmask_b32_e64 v34, 1.0, v210, s[0:1]
	s_waitcnt lgkmcnt(0)
	v_cndmask_b32_e32 v32, v32, v33, vcc
	v_cndmask_b32_e32 v33, v33, v38, vcc
	v_mul_f32_e32 v36, v32, v35
	v_fma_f32 v36, v33, v34, -v36
	v_mul_f32_e32 v33, v33, v35
	v_fmac_f32_e32 v33, v32, v34
	v_mul_f32_e32 v32, v84, v36
	v_mul_f32_e32 v33, v84, v33
	v_cvt_pk_f16_f32 v34, v32, v33
	v_lshl_add_u64 v[32:33], v[48:49], 0, v[70:71]
	global_store_dword v[32:33], v34, off
	v_mov_b32_e32 v32, v41
	v_cndmask_b32_e64 v35, 0, v209, s[0:1]
	v_cndmask_b32_e32 v33, v40, v32, vcc
	ds_bpermute_b32 v33, v169, v33
	v_cndmask_b32_e64 v34, 1.0, v208, s[0:1]
	s_waitcnt lgkmcnt(0)
	v_cndmask_b32_e32 v32, v32, v33, vcc
	v_cndmask_b32_e32 v33, v33, v40, vcc
	v_mul_f32_e32 v36, v32, v35
	v_fma_f32 v36, v33, v34, -v36
	v_mul_f32_e32 v33, v33, v35
	v_fmac_f32_e32 v33, v32, v34
	v_mul_f32_e32 v32, v84, v36
	v_mul_f32_e32 v33, v84, v33
	v_cvt_pk_f16_f32 v34, v32, v33
	v_lshl_add_u64 v[32:33], v[48:49], 0, v[72:73]
	global_store_dword v[32:33], v34, off
	v_mov_b32_e32 v32, v43
	v_cndmask_b32_e64 v35, 0, v207, s[0:1]
	v_cndmask_b32_e32 v33, v42, v32, vcc
	ds_bpermute_b32 v33, v169, v33
	v_cndmask_b32_e64 v34, 1.0, v206, s[0:1]
	s_waitcnt lgkmcnt(0)
	v_cndmask_b32_e32 v32, v32, v33, vcc
	v_cndmask_b32_e32 v33, v33, v42, vcc
	v_mul_f32_e32 v36, v32, v35
	v_fma_f32 v36, v33, v34, -v36
	v_mul_f32_e32 v33, v33, v35
	v_fmac_f32_e32 v33, v32, v34
	v_mul_f32_e32 v32, v84, v36
	v_mul_f32_e32 v33, v84, v33
	v_cvt_pk_f16_f32 v34, v32, v33
	v_lshl_add_u64 v[32:33], v[48:49], 0, v[74:75]
	global_store_dword v[32:33], v34, off
	v_mov_b32_e32 v32, v45
	v_cndmask_b32_e64 v35, 0, v205, s[0:1]
	v_cndmask_b32_e32 v33, v44, v32, vcc
	ds_bpermute_b32 v33, v169, v33
	v_cndmask_b32_e64 v34, 1.0, v204, s[0:1]
	s_waitcnt lgkmcnt(0)
	v_cndmask_b32_e32 v32, v32, v33, vcc
	v_cndmask_b32_e32 v33, v33, v44, vcc
	v_mul_f32_e32 v36, v32, v35
	v_fma_f32 v36, v33, v34, -v36
	v_mul_f32_e32 v33, v33, v35
	v_fmac_f32_e32 v33, v32, v34
	v_mul_f32_e32 v32, v84, v36
	v_mul_f32_e32 v33, v84, v33
	v_cvt_pk_f16_f32 v34, v32, v33
	v_lshl_add_u64 v[32:33], v[48:49], 0, v[76:77]
	global_store_dword v[32:33], v34, off
	v_mov_b32_e32 v32, v47
	s_waitcnt vmcnt(31)
	v_cndmask_b32_e64 v35, 0, v203, s[0:1]
	v_cndmask_b32_e32 v33, v46, v32, vcc
	ds_bpermute_b32 v33, v169, v33
	s_waitcnt lgkmcnt(0)
	v_cndmask_b32_e32 v32, v32, v33, vcc
	v_cndmask_b32_e32 v34, v33, v46, vcc
	v_cndmask_b32_e64 v33, 1.0, v202, s[0:1]
	v_mul_f32_e32 v36, v32, v35
	v_fma_f32 v36, v34, v33, -v36
	v_mul_f32_e32 v34, v34, v35
	v_fmac_f32_e32 v34, v32, v33
	v_mul_f32_e32 v32, v84, v36
	v_mul_f32_e32 v33, v84, v34
	v_cvt_pk_f16_f32 v34, v32, v33
	v_lshl_add_u64 v[32:33], v[48:49], 0, v[78:79]
	global_store_dword v[32:33], v34, off
	s_cselect_b64 s[0:1], -1, 0
	v_cndmask_b32_e32 v32, v16, v17, vcc
	s_and_b32 s2, s2, 0x7ffffc00
	ds_bpermute_b32 v32, v169, v32
	s_cmpk_eq_i32 s2, 0x400
	s_cselect_b32 s2, s6, s12
	s_cselect_b32 s6, s7, s13
	v_cndmask_b32_e64 v34, 1.0, v228, s[0:1]
	s_and_b64 s[0:1], s[0:1], exec
	s_cselect_b32 s5, s5, s6
	s_cselect_b32 s4, s4, s2
	s_cmpk_lt_u32 s14, 0x7c0
	s_cselect_b64 s[0:1], -1, 0
	s_waitcnt lgkmcnt(0)
	v_cndmask_b32_e32 v17, v17, v32, vcc
	v_cndmask_b32_e64 v33, 0, v201, s[0:1]
	v_cndmask_b32_e32 v16, v32, v16, vcc
	v_cndmask_b32_e64 v32, 1.0, v200, s[0:1]
	v_mul_f32_e32 v35, v17, v33
	s_or_b32 s2, s9, s8
	v_fma_f32 v35, v16, v32, -v35
	v_mul_f32_e32 v16, v16, v33
	s_lshl_b64 s[2:3], s[2:3], 18
	v_fmac_f32_e32 v16, v17, v32
	s_add_u32 s2, s4, s2
	v_mul_f32_e32 v17, v34, v35
	v_mul_f32_e32 v16, v34, v16
	s_addc_u32 s3, s5, s3
	v_cvt_pk_f16_f32 v35, v17, v16
	v_lshl_add_u64 v[16:17], s[2:3], 0, v[164:165]
	v_lshl_add_u64 v[32:33], v[16:17], 0, v[80:81]
	global_store_dword v[32:33], v35, off
	v_cndmask_b32_e64 v36, 0, v199, s[0:1]
	v_cndmask_b32_e32 v35, v18, v19, vcc
	ds_bpermute_b32 v35, v169, v35
	s_waitcnt lgkmcnt(0)
	v_cndmask_b32_e32 v19, v19, v35, vcc
	v_cndmask_b32_e32 v18, v35, v18, vcc
	v_cndmask_b32_e64 v35, 1.0, v198, s[0:1]
	v_mul_f32_e32 v37, v19, v36
	v_fma_f32 v37, v18, v35, -v37
	v_mul_f32_e32 v18, v18, v36
	v_fmac_f32_e32 v18, v19, v35
	v_mul_f32_e32 v19, v34, v37
	v_mul_f32_e32 v18, v34, v18
	v_cvt_pk_f16_f32 v18, v19, v18
	global_store_dword v[32:33], v18, off offset:256
	v_mov_b32_e32 v18, v21
	v_cndmask_b32_e64 v21, 0, v197, s[0:1]
	v_cndmask_b32_e32 v19, v20, v18, vcc
	ds_bpermute_b32 v19, v169, v19
	s_waitcnt lgkmcnt(0)
	v_cndmask_b32_e32 v18, v18, v19, vcc
	v_cndmask_b32_e32 v19, v19, v20, vcc
	v_cndmask_b32_e64 v20, 1.0, v196, s[0:1]
	v_mul_f32_e32 v35, v18, v21
	v_fma_f32 v35, v19, v20, -v35
	v_mul_f32_e32 v19, v19, v21
	v_fmac_f32_e32 v19, v18, v20
	v_mul_f32_e32 v18, v34, v35
	v_mul_f32_e32 v19, v34, v19
	v_cvt_pk_f16_f32 v18, v18, v19
	global_store_dword v[32:33], v18, off offset:1024
	v_mov_b32_e32 v18, v23
	v_cndmask_b32_e64 v21, 0, v195, s[0:1]
	v_cndmask_b32_e32 v19, v22, v18, vcc
	ds_bpermute_b32 v19, v169, v19
	v_cndmask_b32_e64 v20, 1.0, v194, s[0:1]
	s_waitcnt lgkmcnt(0)
	v_cndmask_b32_e32 v18, v18, v19, vcc
	v_cndmask_b32_e32 v19, v19, v22, vcc
	v_mul_f32_e32 v22, v18, v21
	v_fma_f32 v22, v19, v20, -v22
	v_mul_f32_e32 v19, v19, v21
	v_fmac_f32_e32 v19, v18, v20
	v_mul_f32_e32 v18, v34, v22
	v_mul_f32_e32 v19, v34, v19
	v_cvt_pk_f16_f32 v18, v18, v19
	global_store_dword v[32:33], v18, off offset:1280
	v_mov_b32_e32 v18, v25
	v_cndmask_b32_e64 v21, 0, v193, s[0:1]
	v_cndmask_b32_e32 v19, v24, v18, vcc
	ds_bpermute_b32 v19, v169, v19
	v_cndmask_b32_e64 v20, 1.0, v192, s[0:1]
	s_waitcnt lgkmcnt(0)
	v_cndmask_b32_e32 v18, v18, v19, vcc
	v_cndmask_b32_e32 v19, v19, v24, vcc
	v_mul_f32_e32 v22, v18, v21
	v_fma_f32 v22, v19, v20, -v22
	v_mul_f32_e32 v19, v19, v21
	v_fmac_f32_e32 v19, v18, v20
	v_mul_f32_e32 v18, v34, v22
	v_mul_f32_e32 v19, v34, v19
	v_cvt_pk_f16_f32 v18, v18, v19
	global_store_dword v[32:33], v18, off offset:2048
	v_mov_b32_e32 v18, v27
	v_cndmask_b32_e64 v21, 0, v191, s[0:1]
	v_cndmask_b32_e32 v19, v26, v18, vcc
	ds_bpermute_b32 v19, v169, v19
	v_cndmask_b32_e64 v20, 1.0, v190, s[0:1]
	s_waitcnt lgkmcnt(0)
	v_cndmask_b32_e32 v18, v18, v19, vcc
	v_cndmask_b32_e32 v19, v19, v26, vcc
	v_mul_f32_e32 v22, v18, v21
	v_fma_f32 v22, v19, v20, -v22
	v_mul_f32_e32 v19, v19, v21
	v_fmac_f32_e32 v19, v18, v20
	v_mul_f32_e32 v18, v34, v22
	v_mul_f32_e32 v19, v34, v19
	v_cvt_pk_f16_f32 v18, v18, v19
	global_store_dword v[32:33], v18, off offset:2304
	v_mov_b32_e32 v18, v29
	v_cndmask_b32_e64 v21, 0, v189, s[0:1]
	v_cndmask_b32_e32 v19, v28, v18, vcc
	ds_bpermute_b32 v19, v169, v19
	v_cndmask_b32_e64 v20, 1.0, v188, s[0:1]
	s_waitcnt lgkmcnt(0)
	v_cndmask_b32_e32 v18, v18, v19, vcc
	v_cndmask_b32_e32 v19, v19, v28, vcc
	v_mul_f32_e32 v22, v18, v21
	v_fma_f32 v22, v19, v20, -v22
	v_mul_f32_e32 v19, v19, v21
	v_fmac_f32_e32 v19, v18, v20
	v_mul_f32_e32 v18, v34, v22
	v_mul_f32_e32 v19, v34, v19
	v_cvt_pk_f16_f32 v18, v18, v19
	global_store_dword v[32:33], v18, off offset:3072
	v_mov_b32_e32 v18, v31
	v_cndmask_b32_e64 v21, 0, v187, s[0:1]
	v_cndmask_b32_e32 v19, v30, v18, vcc
	ds_bpermute_b32 v19, v169, v19
	s_waitcnt lgkmcnt(0)
	v_cndmask_b32_e32 v18, v18, v19, vcc
	v_cndmask_b32_e32 v20, v19, v30, vcc
	v_cndmask_b32_e64 v19, 1.0, v186, s[0:1]
	v_mul_f32_e32 v22, v18, v21
	v_fma_f32 v22, v20, v19, -v22
	v_mul_f32_e32 v20, v20, v21
	v_fmac_f32_e32 v20, v18, v19
	v_mul_f32_e32 v22, v34, v22
	v_mul_f32_e32 v18, v34, v20
	v_cvt_pk_f16_f32 v18, v22, v18
	global_store_dword v[32:33], v18, off offset:3328
	v_cndmask_b32_e64 v19, 0, v185, s[0:1]
	v_cndmask_b32_e32 v18, v0, v1, vcc
	ds_bpermute_b32 v18, v169, v18
	s_waitcnt lgkmcnt(0)
	v_cndmask_b32_e32 v1, v1, v18, vcc
	v_cndmask_b32_e32 v0, v18, v0, vcc
	v_cndmask_b32_e64 v18, 1.0, v184, s[0:1]
	v_mul_f32_e32 v20, v1, v19
	v_fma_f32 v20, v0, v18, -v20
	v_mul_f32_e32 v0, v0, v19
	v_fmac_f32_e32 v0, v1, v18
	v_mul_f32_e32 v20, v34, v20
	v_mul_f32_e32 v0, v34, v0
	v_cvt_pk_f16_f32 v18, v20, v0
	v_lshl_add_u64 v[0:1], v[16:17], 0, v[64:65]
	global_store_dword v[0:1], v18, off
	v_mov_b32_e32 v0, v3
	v_cndmask_b32_e64 v3, 0, v183, s[0:1]
	v_cndmask_b32_e32 v1, v2, v0, vcc
	ds_bpermute_b32 v1, v169, v1
	s_waitcnt lgkmcnt(0)
	v_cndmask_b32_e32 v0, v0, v1, vcc
	v_cndmask_b32_e32 v2, v1, v2, vcc
	v_cndmask_b32_e64 v1, 1.0, v182, s[0:1]
	v_mul_f32_e32 v18, v0, v3
	v_fma_f32 v18, v2, v1, -v18
	v_mul_f32_e32 v2, v2, v3
	v_fmac_f32_e32 v2, v0, v1
	v_mul_f32_e32 v18, v34, v18
	v_mul_f32_e32 v0, v34, v2
	v_cvt_pk_f16_f32 v2, v18, v0
	v_lshl_add_u64 v[0:1], v[16:17], 0, v[66:67]
	global_store_dword v[0:1], v2, off
	v_mov_b32_e32 v0, v5
	v_cndmask_b32_e64 v3, 0, v181, s[0:1]
	v_cndmask_b32_e32 v1, v4, v0, vcc
	ds_bpermute_b32 v1, v169, v1
	s_waitcnt lgkmcnt(0)
	v_cndmask_b32_e32 v0, v0, v1, vcc
	v_cndmask_b32_e32 v2, v1, v4, vcc
	v_cndmask_b32_e64 v1, 1.0, v180, s[0:1]
	v_mul_f32_e32 v4, v0, v3
	v_fma_f32 v4, v2, v1, -v4
	v_mul_f32_e32 v2, v2, v3
	v_fmac_f32_e32 v2, v0, v1
	v_mul_f32_e32 v4, v34, v4
	v_mul_f32_e32 v0, v34, v2
	v_cvt_pk_f16_f32 v2, v4, v0
	v_lshl_add_u64 v[0:1], v[16:17], 0, v[68:69]
	global_store_dword v[0:1], v2, off
	v_mov_b32_e32 v0, v7
	v_cndmask_b32_e64 v3, 0, v179, s[0:1]
	v_cndmask_b32_e32 v1, v6, v0, vcc
	ds_bpermute_b32 v1, v169, v1
	s_waitcnt lgkmcnt(0)
	v_cndmask_b32_e32 v0, v0, v1, vcc
	v_cndmask_b32_e32 v2, v1, v6, vcc
	v_cndmask_b32_e64 v1, 1.0, v178, s[0:1]
	v_mul_f32_e32 v4, v0, v3
	v_fma_f32 v4, v2, v1, -v4
	v_mul_f32_e32 v2, v2, v3
	v_fmac_f32_e32 v2, v0, v1
	v_mul_f32_e32 v4, v34, v4
	v_mul_f32_e32 v0, v34, v2
	v_cvt_pk_f16_f32 v2, v4, v0
	v_lshl_add_u64 v[0:1], v[16:17], 0, v[70:71]
	global_store_dword v[0:1], v2, off
	v_mov_b32_e32 v0, v9
	v_cndmask_b32_e64 v3, 0, v177, s[0:1]
	v_cndmask_b32_e32 v1, v8, v0, vcc
	ds_bpermute_b32 v1, v169, v1
	s_waitcnt lgkmcnt(0)
	v_cndmask_b32_e32 v0, v0, v1, vcc
	v_cndmask_b32_e32 v2, v1, v8, vcc
	v_cndmask_b32_e64 v1, 1.0, v176, s[0:1]
	v_mul_f32_e32 v4, v0, v3
	v_fma_f32 v4, v2, v1, -v4
	v_mul_f32_e32 v2, v2, v3
	v_fmac_f32_e32 v2, v0, v1
	v_mul_f32_e32 v4, v34, v4
	v_mul_f32_e32 v0, v34, v2
	v_cvt_pk_f16_f32 v2, v4, v0
	v_lshl_add_u64 v[0:1], v[16:17], 0, v[72:73]
	global_store_dword v[0:1], v2, off
	v_mov_b32_e32 v0, v11
	v_cndmask_b32_e64 v3, 0, v175, s[0:1]
	v_cndmask_b32_e32 v1, v10, v0, vcc
	ds_bpermute_b32 v1, v169, v1
	s_waitcnt lgkmcnt(0)
	v_cndmask_b32_e32 v0, v0, v1, vcc
	v_cndmask_b32_e32 v2, v1, v10, vcc
	v_cndmask_b32_e64 v1, 1.0, v174, s[0:1]
	v_mul_f32_e32 v4, v0, v3
	v_fma_f32 v4, v2, v1, -v4
	v_mul_f32_e32 v2, v2, v3
	v_fmac_f32_e32 v2, v0, v1
	v_mul_f32_e32 v4, v34, v4
	v_mul_f32_e32 v0, v34, v2
	v_cvt_pk_f16_f32 v2, v4, v0
	v_lshl_add_u64 v[0:1], v[16:17], 0, v[74:75]
	global_store_dword v[0:1], v2, off
	v_mov_b32_e32 v0, v13
	v_cndmask_b32_e64 v3, 0, v173, s[0:1]
	v_cndmask_b32_e32 v1, v12, v0, vcc
	ds_bpermute_b32 v1, v169, v1
	s_waitcnt lgkmcnt(0)
	v_cndmask_b32_e32 v0, v0, v1, vcc
	v_cndmask_b32_e32 v2, v1, v12, vcc
	v_cndmask_b32_e64 v1, 1.0, v172, s[0:1]
	v_mul_f32_e32 v4, v0, v3
	v_fma_f32 v4, v2, v1, -v4
	v_mul_f32_e32 v2, v2, v3
	v_fmac_f32_e32 v2, v0, v1
	v_mul_f32_e32 v4, v34, v4
	v_mul_f32_e32 v0, v34, v2
	v_cvt_pk_f16_f32 v2, v4, v0
	v_lshl_add_u64 v[0:1], v[16:17], 0, v[76:77]
	global_store_dword v[0:1], v2, off
	v_mov_b32_e32 v0, v15
	v_cndmask_b32_e64 v3, 0, v171, s[0:1]
	v_cndmask_b32_e32 v1, v14, v0, vcc
	ds_bpermute_b32 v1, v169, v1
	v_cndmask_b32_e64 v2, 1.0, v170, s[0:1]
	s_waitcnt lgkmcnt(0)
	v_cndmask_b32_e32 v0, v0, v1, vcc
	v_cndmask_b32_e32 v1, v1, v14, vcc
	v_mul_f32_e32 v4, v0, v3
	v_fma_f32 v4, v1, v2, -v4
	v_mul_f32_e32 v1, v1, v3
	v_fmac_f32_e32 v1, v0, v2
	v_mul_f32_e32 v4, v34, v4
	v_mul_f32_e32 v0, v34, v1
	v_cvt_pk_f16_f32 v2, v4, v0
	v_lshl_add_u64 v[0:1], v[16:17], 0, v[78:79]
	global_store_dword v[0:1], v2, off
	s_endpgm
	.p2alignl 8, 3212836864

	.amdhsa_kernel _Z11gemm_kernelILi256ELi192ELi4ELi2ELi0EEvPKDF16_S1_PKfS3_PDF16_S4_S4_Pfi
		.amdhsa_group_segment_fixed_size 0
		.amdhsa_private_segment_fixed_size 0
		.amdhsa_kernarg_size 68
		.amdhsa_user_sgpr_count 2
		.amdhsa_user_sgpr_dispatch_ptr 0
		.amdhsa_user_sgpr_queue_ptr 0
		.amdhsa_user_sgpr_kernarg_segment_ptr 1
		.amdhsa_user_sgpr_dispatch_id 0
		.amdhsa_user_sgpr_kernarg_preload_length 0
		.amdhsa_user_sgpr_kernarg_preload_offset 0
		.amdhsa_user_sgpr_private_segment_size 0
		.amdhsa_uses_dynamic_stack 0
		.amdhsa_enable_private_segment 0
		.amdhsa_system_sgpr_workgroup_id_x 1
		.amdhsa_system_sgpr_workgroup_id_y 0
		.amdhsa_system_sgpr_workgroup_id_z 0
		.amdhsa_system_sgpr_workgroup_info 0
		.amdhsa_system_vgpr_workitem_id 0
		.amdhsa_next_free_vgpr 249
		.amdhsa_next_free_sgpr 24
		.amdhsa_accum_offset 252
		.amdhsa_reserve_vcc 1
		.amdhsa_float_round_mode_32 0
		.amdhsa_float_round_mode_16_64 0
		.amdhsa_float_denorm_mode_32 3
		.amdhsa_float_denorm_mode_16_64 3
		.amdhsa_dx10_clamp 1
		.amdhsa_ieee_mode 1
		.amdhsa_fp16_overflow 0
		.amdhsa_tg_split 0
		.amdhsa_exception_fp_ieee_invalid_op 0
		.amdhsa_exception_fp_denorm_src 0
		.amdhsa_exception_fp_ieee_div_zero 0
		.amdhsa_exception_fp_ieee_overflow 0
		.amdhsa_exception_fp_ieee_underflow 0
		.amdhsa_exception_fp_ieee_inexact 0
		.amdhsa_exception_int_div_zero 0
	.end_amdhsa_kernel
